# adds: XCD-aware unit permutation in P7/P8, ACT stored k-block-major, P5 conversion block rewritten (adjacent tile pairs, 2 in flight)
# speedup vs baseline: 1.0107x; 1.0107x over previous
; __device__ __forceinline__ void conv8_fill(const Ctx& X, int base, int rank, int nblk, int n) { conv8b_run(X, (base >> 3) + rank, nblk, n); }
; #define SEAM(k) do { if (IN(k) && IN((k) + 1)) xcd_barrier(bar); } while (0)
; __device__ __forceinline__ void conv8b_run(const Ctx& X, int first, int step, int count) {
;     if (count <= 0) return;
;     f32x4 v[16];
;     Cvb c = conv8b_dec(X, first), cn = c;
; #pragma unroll
;     for (int i = 0; i < 16; ++i) v[i] = __builtin_nontemporal_load((const f32x4*)(c.W + (size_t)i * c.N));
; __global__ void __launch_bounds__(NTHR, 2) fwd(Args args) {
;     ...
;     if (IN(5)) {
;         const int gb = (X.G == 256) ? P5_GEMM_BLOCKS : X.G;
;         if (X.bid < gb) { DenseSched S{(const char*)XP_MIX(X), (const char*)XP_WoutT(X), 64, T / 256, D / 256, (T / 256) * (D / 256), gb, X.bid}; EpiOut E{XP_x(X), XP_Hh(X)};
;             pg8::gemm_phase<EpiOut, DenseSched, false, false>(X.lds, D, 64, 64, (size_t)PANE_A * 2, (size_t)PANE_WOUT * 2, S, E); }
;         else conv8_fill(X, Q5_BASE, X.bid - gb, Q5_W / NWAVES, Q5_N); } SEAM(5);
.LBB0_721:
	s_cmp_lt_i32 s94, 6
	s_cselect_b64 s[4:5], -1, 0
	s_and_b64 s[2:3], s[4:5], s[2:3]
	s_andn2_b64 vcc, exec, s[2:3]
	s_cbranch_vccnz .LBB0_762
	s_cmpk_lg_i32 s92, 0x100
	s_cselect_b32 s30, s92, 0x80
	s_cmp_ge_i32 s87, s30
	s_mov_b64 s[4:5], -1
	s_cbranch_scc0 .LBB0_737
	s_load_dwordx2 s[6:7], s[0:1], 0x70
	s_load_dwordx2 s[8:9], s[0:1], 0x80
	s_sub_i32 s18, s87, s30
	s_lshl_b32 s18, s18, 1
	s_add_i32 s18, s18, 0x1dc0
	s_mov_b32 s19, 24
	s_mov_b32 s24, 0xc3e00000
	v_mov_b32_e32 v150, 0x43e00000
	v_lshlrev_b32_e32 v146, 4, v194
	v_mul_u32_u24_e32 v147, 0x240, v194
	s_lshl_b32 s20, s93, 4
	v_add_u32_e32 v147, s20, v147
	v_lshrrev_b32_e32 v151, 3, v194
	s_lshl_b32 s20, s93, 5
	v_add_u32_e32 v152, s20, v151
	v_mul_u32_u24_e32 v148, 0x90, v152
	v_and_b32_e32 v152, 7, v194
	v_lshl_add_u32 v148, v152, 4, v148
	v_lshlrev_b32_e32 v151, 7, v151
	v_lshl_add_u32 v149, v152, 4, v151
	s_waitcnt lgkmcnt(0)
	s_add_i32 s27, s18, 1
	s_cmp_lt_u32 s18, 0x2000
	s_cbranch_scc0 .Lcv5_dnP0
	s_lshr_b32 s20, s18, 4
	s_lshl_b32 s20, s20, 21
	s_and_b32 s21, s18, 15
	s_lshl_b32 s21, s21, 10
	s_add_u32 s20, s20, s21
	s_lshl_b32 s21, s93, 18
	s_add_u32 s20, s20, s21
	s_add_u32 s10, s6, s20
	s_addc_u32 s11, s7, 0
	s_movk_i32 s12, 0x4000
	s_lshl_b32 s20, s18, 15
	s_add_u32 s20, s20, 0x30000000
	s_branch .Lcv5_cmP0

; __device__ __forceinline__ Cvb conv8b_dec(const Ctx& X, int bit) { Cvb c; int kb, nb;
;     if (bit < I_GU8 / 8) { const int e = bit >> 8, r = bit & 255; kb = r >> 4; nb = r & 15; c.N = 2 * DFF; c.W = XP_w_gu(X) + (size_t)e * D * (2 * DFF); c.WT = XP_WguT(X) + (size_t)e * 16 * PAN_GU + (size_t)kb * PAN_GU; }
;     else { const int b2 = bit - I_GU8 / 8, e = b2 >> 7, r = b2 & 127; kb = r >> 3; nb = r & 7; c.N = D; c.W = XP_w_d(X) + (size_t)e * DFF * D; c.WT = XP_WdT(X) + (size_t)e * 16 * PAN_D + (size_t)kb * PAN_D; }
;     c.W += (size_t)(kb * 128 + 16 * X.wave) * c.N + nb * 256 + 4 * X.lane;
;     c.WT += (size_t)(nb * 256 + 32 * X.wave + (X.lane >> 3)) * 128 + 16 * (X.lane & 7);
;     return c; }
; __device__ __forceinline__ void conv8b_run(const Ctx& X, int first, int step, int count) {
;     if (count <= 0) return;
;     f32x4 v[16];
;     Cvb c = conv8b_dec(X, first), cn = c;
; #pragma unroll
;     for (int i = 0; i < 16; ++i) v[i] = __builtin_nontemporal_load((const f32x4*)(c.W + (size_t)i * c.N));
.Lcv5_cmP0:
	s_lshl_b32 s21, s93, 12
	s_add_u32 s20, s20, s21
	s_add_u32 s14, s90, s20
	s_addc_u32 s15, s91, 0
	global_load_dwordx4 v[2:5], v146, s[10:11] nt
	s_add_u32 s10, s10, s12
	s_addc_u32 s11, s11, 0
	global_load_dwordx4 v[6:9], v146, s[10:11] nt
	s_add_u32 s10, s10, s12
	s_addc_u32 s11, s11, 0
	global_load_dwordx4 v[10:13], v146, s[10:11] nt
	s_add_u32 s10, s10, s12
	s_addc_u32 s11, s11, 0
	global_load_dwordx4 v[14:17], v146, s[10:11] nt
	s_add_u32 s10, s10, s12
	s_addc_u32 s11, s11, 0
	global_load_dwordx4 v[18:21], v146, s[10:11] nt
	s_add_u32 s10, s10, s12
	s_addc_u32 s11, s11, 0
	global_load_dwordx4 v[22:25], v146, s[10:11] nt
	s_add_u32 s10, s10, s12
	s_addc_u32 s11, s11, 0
	global_load_dwordx4 v[26:29], v146, s[10:11] nt
	s_add_u32 s10, s10, s12
	s_addc_u32 s11, s11, 0
	global_load_dwordx4 v[30:33], v146, s[10:11] nt
	s_add_u32 s10, s10, s12
	s_addc_u32 s11, s11, 0
	global_load_dwordx4 v[34:37], v146, s[10:11] nt
	s_add_u32 s10, s10, s12
	s_addc_u32 s11, s11, 0
	global_load_dwordx4 v[38:41], v146, s[10:11] nt
	s_add_u32 s10, s10, s12
	s_addc_u32 s11, s11, 0
	global_load_dwordx4 v[42:45], v146, s[10:11] nt
	s_add_u32 s10, s10, s12
	s_addc_u32 s11, s11, 0
	global_load_dwordx4 v[46:49], v146, s[10:11] nt
	s_add_u32 s10, s10, s12
	s_addc_u32 s11, s11, 0
	global_load_dwordx4 v[50:53], v146, s[10:11] nt
	s_add_u32 s10, s10, s12
	s_addc_u32 s11, s11, 0
	global_load_dwordx4 v[54:57], v146, s[10:11] nt
	s_add_u32 s10, s10, s12
	s_addc_u32 s11, s11, 0
	global_load_dwordx4 v[58:61], v146, s[10:11] nt
	s_add_u32 s10, s10, s12
	s_addc_u32 s11, s11, 0
	global_load_dwordx4 v[62:65], v146, s[10:11] nt
	s_add_i32 s18, s18, 256
	s_add_i32 s19, s19, -1
	s_mov_b32 s25, 0
	s_cmp_eq_u32 s19, 0
	s_cbranch_scc1 .Lcv5_loop
	s_cmp_lt_u32 s27, 0x2000
	s_cbranch_scc0 .Lcv5_dnP1
	s_lshr_b32 s20, s27, 4
	s_lshl_b32 s20, s20, 21
	s_and_b32 s21, s27, 15
	s_lshl_b32 s21, s21, 10
	s_add_u32 s20, s20, s21
	s_lshl_b32 s21, s93, 18
	s_add_u32 s20, s20, s21
	s_add_u32 s10, s6, s20
	s_addc_u32 s11, s7, 0
	s_movk_i32 s12, 0x4000
	s_lshl_b32 s20, s27, 15
	s_add_u32 s20, s20, 0x30000000
	s_branch .Lcv5_cmP1

; __device__ __forceinline__ Cvb conv8b_dec(const Ctx& X, int bit) { Cvb c; int kb, nb;
;     if (bit < I_GU8 / 8) { const int e = bit >> 8, r = bit & 255; kb = r >> 4; nb = r & 15; c.N = 2 * DFF; c.W = XP_w_gu(X) + (size_t)e * D * (2 * DFF); c.WT = XP_WguT(X) + (size_t)e * 16 * PAN_GU + (size_t)kb * PAN_GU; }
;     else { const int b2 = bit - I_GU8 / 8, e = b2 >> 7, r = b2 & 127; kb = r >> 3; nb = r & 7; c.N = D; c.W = XP_w_d(X) + (size_t)e * DFF * D; c.WT = XP_WdT(X) + (size_t)e * 16 * PAN_D + (size_t)kb * PAN_D; }
;     c.W += (size_t)(kb * 128 + 16 * X.wave) * c.N + nb * 256 + 4 * X.lane;
;     c.WT += (size_t)(nb * 256 + 32 * X.wave + (X.lane >> 3)) * 128 + 16 * (X.lane & 7);
;     return c; }
; __device__ __forceinline__ void conv8b_run(const Ctx& X, int first, int step, int count) {
;     if (count <= 0) return;
;     f32x4 v[16];
;     Cvb c = conv8b_dec(X, first), cn = c;
; #pragma unroll
;     for (int i = 0; i < 16; ++i) v[i] = __builtin_nontemporal_load((const f32x4*)(c.W + (size_t)i * c.N));
.Lcv5_cmP1:
	s_lshl_b32 s21, s93, 12
	s_add_u32 s20, s20, s21
	s_add_u32 s16, s90, s20
	s_addc_u32 s17, s91, 0
	global_load_dwordx4 v[66:69], v146, s[10:11] nt
	s_add_u32 s10, s10, s12
	s_addc_u32 s11, s11, 0
	global_load_dwordx4 v[70:73], v146, s[10:11] nt
	s_add_u32 s10, s10, s12
	s_addc_u32 s11, s11, 0
	global_load_dwordx4 v[74:77], v146, s[10:11] nt
	s_add_u32 s10, s10, s12
	s_addc_u32 s11, s11, 0
	global_load_dwordx4 v[78:81], v146, s[10:11] nt
	s_add_u32 s10, s10, s12
	s_addc_u32 s11, s11, 0
	global_load_dwordx4 v[82:85], v146, s[10:11] nt
	s_add_u32 s10, s10, s12
	s_addc_u32 s11, s11, 0
	global_load_dwordx4 v[86:89], v146, s[10:11] nt
	s_add_u32 s10, s10, s12
	s_addc_u32 s11, s11, 0
	global_load_dwordx4 v[90:93], v146, s[10:11] nt
	s_add_u32 s10, s10, s12
	s_addc_u32 s11, s11, 0
	global_load_dwordx4 v[94:97], v146, s[10:11] nt
	s_add_u32 s10, s10, s12
	s_addc_u32 s11, s11, 0
	global_load_dwordx4 v[98:101], v146, s[10:11] nt
	s_add_u32 s10, s10, s12
	s_addc_u32 s11, s11, 0
	global_load_dwordx4 v[102:105], v146, s[10:11] nt
	s_add_u32 s10, s10, s12
	s_addc_u32 s11, s11, 0
	global_load_dwordx4 v[106:109], v146, s[10:11] nt
	s_add_u32 s10, s10, s12
	s_addc_u32 s11, s11, 0
	global_load_dwordx4 v[110:113], v146, s[10:11] nt
	s_add_u32 s10, s10, s12
	s_addc_u32 s11, s11, 0
	global_load_dwordx4 v[114:117], v146, s[10:11] nt
	s_add_u32 s10, s10, s12
	s_addc_u32 s11, s11, 0
	global_load_dwordx4 v[118:121], v146, s[10:11] nt
	s_add_u32 s10, s10, s12
	s_addc_u32 s11, s11, 0
	global_load_dwordx4 v[122:125], v146, s[10:11] nt
	s_add_u32 s10, s10, s12
	s_addc_u32 s11, s11, 0
	global_load_dwordx4 v[126:129], v146, s[10:11] nt
	s_add_i32 s27, s27, 256
	s_add_i32 s19, s19, -1
	s_mov_b32 s25, 1
	s_waitcnt vmcnt(16)

; __device__ __forceinline__ void conv8b_run(const Ctx& X, int first, int step, int count) {
;     ...
;         if (j + 1 < count) { cn = conv8b_dec(X, first + (j + 1) * step);
; #pragma unroll
;             for (int i = 0; i < 16; ++i) v[i] = __builtin_nontemporal_load((const f32x4*)(cn.W + (size_t)i * cn.N)); }
.Lcv5_cmLA:
	s_lshl_b32 s21, s93, 12
	s_add_u32 s20, s20, s21
	s_add_u32 s14, s90, s20
	s_addc_u32 s15, s91, 0
	global_load_dwordx4 v[2:5], v146, s[10:11] nt
	s_add_u32 s10, s10, s12
	s_addc_u32 s11, s11, 0
	global_load_dwordx4 v[6:9], v146, s[10:11] nt
	s_add_u32 s10, s10, s12
	s_addc_u32 s11, s11, 0
	global_load_dwordx4 v[10:13], v146, s[10:11] nt
	s_add_u32 s10, s10, s12
	s_addc_u32 s11, s11, 0
	global_load_dwordx4 v[14:17], v146, s[10:11] nt
	s_add_u32 s10, s10, s12
	s_addc_u32 s11, s11, 0
	global_load_dwordx4 v[18:21], v146, s[10:11] nt
	s_add_u32 s10, s10, s12
	s_addc_u32 s11, s11, 0
	global_load_dwordx4 v[22:25], v146, s[10:11] nt
	s_add_u32 s10, s10, s12
	s_addc_u32 s11, s11, 0
	global_load_dwordx4 v[26:29], v146, s[10:11] nt
	s_add_u32 s10, s10, s12
	s_addc_u32 s11, s11, 0
	global_load_dwordx4 v[30:33], v146, s[10:11] nt
	s_add_u32 s10, s10, s12
	s_addc_u32 s11, s11, 0
	global_load_dwordx4 v[34:37], v146, s[10:11] nt
	s_add_u32 s10, s10, s12
	s_addc_u32 s11, s11, 0
	global_load_dwordx4 v[38:41], v146, s[10:11] nt
	s_add_u32 s10, s10, s12
	s_addc_u32 s11, s11, 0
	global_load_dwordx4 v[42:45], v146, s[10:11] nt
	s_add_u32 s10, s10, s12
	s_addc_u32 s11, s11, 0
	global_load_dwordx4 v[46:49], v146, s[10:11] nt
	s_add_u32 s10, s10, s12
	s_addc_u32 s11, s11, 0
	global_load_dwordx4 v[50:53], v146, s[10:11] nt
	s_add_u32 s10, s10, s12
	s_addc_u32 s11, s11, 0
	global_load_dwordx4 v[54:57], v146, s[10:11] nt
	s_add_u32 s10, s10, s12
	s_addc_u32 s11, s11, 0
	global_load_dwordx4 v[58:61], v146, s[10:11] nt
	s_add_u32 s10, s10, s12
	s_addc_u32 s11, s11, 0
	global_load_dwordx4 v[62:65], v146, s[10:11] nt
	s_add_i32 s18, s18, 256
	s_add_i32 s19, s19, -1
	s_branch .Lcv5_nxA

; __device__ __forceinline__ void conv8b_run(const Ctx& X, int first, int step, int count) {
;     ...
;         if (j + 1 < count) { cn = conv8b_dec(X, first + (j + 1) * step);
; #pragma unroll
;             for (int i = 0; i < 16; ++i) v[i] = __builtin_nontemporal_load((const f32x4*)(cn.W + (size_t)i * cn.N)); }
.Lcv5_cmLB:
	s_lshl_b32 s21, s93, 12
	s_add_u32 s20, s20, s21
	s_add_u32 s16, s90, s20
	s_addc_u32 s17, s91, 0
	global_load_dwordx4 v[66:69], v146, s[10:11] nt
	s_add_u32 s10, s10, s12
	s_addc_u32 s11, s11, 0
	global_load_dwordx4 v[70:73], v146, s[10:11] nt
	s_add_u32 s10, s10, s12
	s_addc_u32 s11, s11, 0
	global_load_dwordx4 v[74:77], v146, s[10:11] nt
	s_add_u32 s10, s10, s12
	s_addc_u32 s11, s11, 0
	global_load_dwordx4 v[78:81], v146, s[10:11] nt
	s_add_u32 s10, s10, s12
	s_addc_u32 s11, s11, 0
	global_load_dwordx4 v[82:85], v146, s[10:11] nt
	s_add_u32 s10, s10, s12
	s_addc_u32 s11, s11, 0
	global_load_dwordx4 v[86:89], v146, s[10:11] nt
	s_add_u32 s10, s10, s12
	s_addc_u32 s11, s11, 0
	global_load_dwordx4 v[90:93], v146, s[10:11] nt
	s_add_u32 s10, s10, s12
	s_addc_u32 s11, s11, 0
	global_load_dwordx4 v[94:97], v146, s[10:11] nt
	s_add_u32 s10, s10, s12
	s_addc_u32 s11, s11, 0
	global_load_dwordx4 v[98:101], v146, s[10:11] nt
	s_add_u32 s10, s10, s12
	s_addc_u32 s11, s11, 0
	global_load_dwordx4 v[102:105], v146, s[10:11] nt
	s_add_u32 s10, s10, s12
	s_addc_u32 s11, s11, 0
	global_load_dwordx4 v[106:109], v146, s[10:11] nt
	s_add_u32 s10, s10, s12
	s_addc_u32 s11, s11, 0
	global_load_dwordx4 v[110:113], v146, s[10:11] nt
	s_add_u32 s10, s10, s12
	s_addc_u32 s11, s11, 0
	global_load_dwordx4 v[114:117], v146, s[10:11] nt
	s_add_u32 s10, s10, s12
	s_addc_u32 s11, s11, 0
	global_load_dwordx4 v[118:121], v146, s[10:11] nt
	s_add_u32 s10, s10, s12
	s_addc_u32 s11, s11, 0
	global_load_dwordx4 v[122:125], v146, s[10:11] nt
	s_add_u32 s10, s10, s12
	s_addc_u32 s11, s11, 0
	global_load_dwordx4 v[126:129], v146, s[10:11] nt
	s_add_i32 s27, s27, 256
	s_add_i32 s19, s19, -1
	s_branch .Lcv5_nxB

; __device__ __forceinline__ void conv8b_run(const Ctx& X, int first, int step, int count) {
;     ...
;     asm volatile("s_waitcnt lgkmcnt(0)" ::: "memory"); __builtin_amdgcn_s_barrier();
; }
.Lcv5_done:
	s_mov_b64 s[4:5], 0
	s_waitcnt lgkmcnt(0)
	s_barrier

; template <class Epi, class Sched, bool GATHER, bool FP8>
; __device__ __forceinline__ void gemm_phase(LAS uchar* lds, const int K, const int LDA, const int LDB, const size_t kstepA, const size_t kstepB, const Sched& S, const Epi& E) {
;     ...
;     Unit cur, nxt; int ui = 0;
;     if (!S.next(0, cur)) return;
;     f32x4 acc[2][2][4][2];
; #pragma unroll
;     for (int a = 0; a < 2; ++a)
; #pragma unroll
;         for (int b = 0; b < 2; ++b)
; #pragma unroll
;             for (int m = 0; m < 4; ++m)
; #pragma unroll
;                 for (int n = 0; n < 2; ++n) acc[a][b][m][n] = (f32x4){0.f, 0.f, 0.f, 0.f};
;     bf16x8 At[4][2], B0[2][2], B1[2][2];
;     const char* cA = cur.pa; const char* cB = cur.pb;
;     if constexpr (GATHER) S.gather(cur, voA, (const LAS int*)nullptr);
;     PG8_STAGE(PG8_SB(0, 0), cB, voffB); PG8_STAGE(PG8_SB(0, 1), cB + hstep, voffB); PG8_STAGE(PG8_SA(0, 0), cA, voA[0]); PG8_STAGE(PG8_SA(0, 1), cA, voA[1]);
;     if (wr == 1) PG8_BAR;
;     PG8_WAIT_V(2); PG8_BAR;
;     PG8_STAGE(PG8_SB(1, 0), cB + kstepB, voffB); PG8_STAGE(PG8_SA(1, 0), cA + kstepA, voA[0]); PG8_STAGE(PG8_SB(1, 1), cB + hstep + kstepB, voffB);
;     PG8_WAIT_V(6); PG8_BAR;
;     __device__ __forceinline__ bool next(int i, pg8::Unit& u) const {
;         const int NB = __builtin_amdgcn_readfirstlane(tab[0]); const int L = i * G + c; if (L >= NB * nN) return false;
;         const int b = L / nN, pn = L - b * nN, e = __builtin_amdgcn_readfirstlane(tab[64 + b]);
;         u.pa = A; u.pb = B + (size_t)e * bexp + (size_t)pn * 256 * 128; u.row0 = b * 256; u.col0 = pn * 256; u.aux = e; u.blk = b; return true;
;     }
;     __device__ __forceinline__ void prefetch(const pg8::Unit& u, LAS uchar* buf, int wid, int lane) const {
;         { const int e = u.aux, lb = (u.blk - __builtin_amdgcn_readfirstlane(tab[8 + e])) * 256, w4 = wid & 3;
;             __builtin_amdgcn_global_load_lds((const unsigned*)(list + e * T + lb + 64 * w4 + lane), (LAS unsigned*)(buf + w4 * 256), 4, 0, 0); }
;     }
;     __device__ __forceinline__ void gather(const pg8::Unit& u, unsigned (&vo)[2][2], const LAS int* idx) const {
;         const int e = u.aux, lb = (u.blk - __builtin_amdgcn_readfirstlane(tab[8 + e])) * 256, cnt = __builtin_amdgcn_readfirstlane(tab[256 + u.blk]);
; #pragma unroll
;         for (int i = 0; i < 2; ++i) { int R, C; pg8::stage_rc((int)threadIdx.x * 16 + i * 8192, R, C);
.LBB0_917:
	s_or_b64 exec, exec, s[8:9]
	s_add_i32 s12, 0, 0x22000
	s_waitcnt vmcnt(4)
	v_mov_b32_e32 v2, s12
	s_waitcnt lgkmcnt(0)
	s_barrier
	ds_read_b32 v2, v2
	v_readfirstlane_b32 s20, v0
	s_waitcnt lgkmcnt(0)
	v_readfirstlane_b32 s2, v2
	s_lshl_b32 s2, s2, 4
	s_and_b32 s99, s87, 3
	s_lshl_b32 s98, s99, 6
	s_lshr_b32 s99, s87, 6
	s_lshl_b32 s99, s99, 4
	s_or_b32 s98, s98, s99
	s_bfe_u32 s99, s87, 0x10002
	s_lshl_b32 s99, s99, 3
	s_or_b32 s98, s98, s99
	s_bfe_u32 s99, s87, 0x30003
	s_or_b32 s98, s98, s99
	s_cmpk_eq_i32 s92, 0x100
	s_cselect_b32 s98, s98, s87
	s_cmp_ge_i32 s98, s2
	s_cbranch_scc1 .LBB0_937
	s_add_u32 s8, s90, 0x6000000
	s_addc_u32 s9, s91, 0
	s_add_u32 s25, s90, 0x30000000
	s_addc_u32 s33, s91, 0
	s_add_u32 s10, s90, 0x2f00000
	s_addc_u32 s11, s91, 0
	s_ashr_i32 s2, s98, 31
	s_lshr_b32 s2, s2, 28
	s_add_i32 s2, s98, s2
	s_ashr_i32 s18, s2, 4
	s_lshl_b32 s3, s18, 2
	s_add_i32 s3, s12, s3
	v_mov_b32_e32 v2, s3
	ds_read2st64_b32 v[2:3], v2 offset0:1 offset1:4
	s_lshr_b32 s21, s20, 6
	s_and_b32 s2, s2, -16
	s_lshr_b32 s22, s20, 8
	s_lshl_b32 s52, s21, 10
	s_waitcnt lgkmcnt(0)
	v_readfirstlane_b32 s42, v2
	s_ashr_i32 s43, s42, 31
	s_sub_i32 s2, s98, s2
	s_lshl_b64 s[14:15], s[42:43], 23
	s_add_u32 s13, s25, s14
	s_addc_u32 s16, s33, s15
	s_ashr_i32 s3, s2, 31
	s_lshl_b64 s[14:15], s[2:3], 15
	s_add_u32 s44, s13, s14
	s_addc_u32 s45, s16, s15
	s_lshl_b32 s3, s42, 2
	s_add_i32 s3, s12, s3
	v_mov_b32_e32 v2, s3
	ds_read_b32 v2, v2 offset:32
	v_lshrrev_b32_e32 v13, 3, v0
	v_bfe_u32 v12, v0, 2, 4
	v_or_b32_e32 v4, 64, v13
	s_movk_i32 s3, 0x70
	v_and_or_b32 v195, v4, s3, v12
	s_waitcnt lgkmcnt(0)
	v_readfirstlane_b32 s3, v2
	s_sub_i32 s3, s18, s3
	s_lshl_b32 s3, s3, 8
	s_lshl_b32 s12, s42, 13
	s_add_i32 s3, s3, s12
	v_and_or_b32 v208, v13, 48, v12
	v_or_b32_e32 v4, s3, v208
	v_or_b32_e32 v209, 0x80, v208
	v_or_b32_e32 v210, 0x80, v195
	v_ashrrev_i32_e32 v5, 31, v4
	v_or_b32_e32 v6, s3, v209
	v_or_b32_e32 v8, s3, v195
	v_or_b32_e32 v10, s3, v210
	v_lshl_add_u64 v[4:5], v[4:5], 2, s[10:11]
	v_ashrrev_i32_e32 v7, 31, v6
	v_ashrrev_i32_e32 v9, 31, v8
	v_ashrrev_i32_e32 v11, 31, v10
	v_lshl_add_u64 v[6:7], v[6:7], 2, s[10:11]
	v_lshl_add_u64 v[8:9], v[8:9], 2, s[10:11]
	v_lshl_add_u64 v[10:11], v[10:11], 2, s[10:11]
	global_load_dword v14, v[4:5], off
	global_load_dword v15, v[6:7], off
	global_load_dword v16, v[8:9], off
	global_load_dword v17, v[10:11], off
	v_lshlrev_b32_e32 v4, 4, v0
	v_and_b32_e32 v5, 32, v0
	v_bitop3_b32 v4, v4, v5, 48 bitop3:0x6c
	v_and_or_b32 v5, v13, 32, v12
	v_and_b32_e32 v2, 48, v0
	s_movk_i32 s14, 0x46
	v_and_or_b32 v211, v0, 64, v4
	v_lshlrev_b32_e32 v4, 1, v5
	s_movk_i32 s3, 0xc6
	v_lshlrev_b32_e32 v5, 1, v195
	v_and_or_b32 v4, v4, s14, v2
	s_add_i32 s53, s52, 0
	v_and_b32_e32 v6, 0x80, v0
	v_mov_b32_e32 v197, 0
	v_and_or_b32 v5, v5, s3, v2
	v_lshlrev_b32_e32 v4, 7, v4
	s_add_i32 s54, s53, 0x10000
	v_mov_b32_e32 v199, v197
	v_lshlrev_b32_e32 v5, 7, v5
	v_or3_b32 v198, v4, v6, v211
	s_add_i32 s55, s53, 0x12000
	s_mov_b32 m0, s54
	s_mov_b64 s[12:13], 0x400
	v_or3_b32 v200, v5, v6, v211
	v_readfirstlane_b32 s3, v3
	v_lshl_add_u64 v[4:5], s[44:45], 0, v[198:199]
	s_add_i32 s56, s53, 0x14000
	global_load_lds_dwordx4 v198, s[44:45]
	s_mov_b32 m0, s55
	v_mov_b32_e32 v201, v197
	v_lshl_add_u64 v[4:5], v[4:5], 0, s[12:13]
	global_load_lds_dwordx4 v200, s[44:45]
	s_mov_b32 m0, s56
	v_cmp_gt_i32_e32 vcc, s3, v208
	v_lshl_add_u64 v[6:7], s[44:45], 0, v[200:201]
	s_add_i32 s57, s53, 0x16000
	global_load_lds_dwordx4 v[4:5], off
	v_lshl_add_u64 v[6:7], v[6:7], 0, s[12:13]
	s_mov_b32 m0, s57
	s_add_i32 s58, s53, 0x2000
	global_load_lds_dwordx4 v[6:7], off
	s_mov_b32 m0, s53
	s_add_i32 s59, s53, 0x4000
	s_add_i32 s60, s53, 0x6000
	s_load_dwordx2 s[14:15], s[0:1], 0x78
	s_cmp_eq_u32 s22, 1
	s_mov_b32 s46, 0
	s_cselect_b64 s[16:17], -1, 0
	s_cmp_lg_u32 s22, 1
	v_mov_b32_e32 v203, v197
	s_waitcnt vmcnt(0)
	v_lshlrev_b32_e32 v3, 11, v14
	v_lshlrev_b32_e32 v4, 11, v15
	v_cndmask_b32_e32 v3, 0, v3, vcc
	v_cmp_gt_i32_e32 vcc, s3, v209
	v_lshlrev_b32_e32 v5, 11, v16
	v_or_b32_e32 v196, v3, v211
	v_cndmask_b32_e32 v4, 0, v4, vcc
	v_cmp_gt_i32_e32 vcc, s3, v195
	v_lshlrev_b32_e32 v6, 11, v17
	global_load_lds_dwordx4 v196, s[8:9]
	v_cndmask_b32_e32 v5, 0, v5, vcc
	v_cmp_gt_i32_e32 vcc, s3, v210
	v_or_b32_e32 v202, v5, v211
	s_mov_b32 m0, s58
	v_cndmask_b32_e32 v6, 0, v6, vcc
	v_or_b32_e32 v3, v4, v211
	global_load_lds_dwordx4 v202, s[8:9]
	s_mov_b32 m0, s59
	v_or_b32_e32 v204, v6, v211
	global_load_lds_dwordx4 v3, s[8:9]
	s_mov_b32 m0, s60
	s_nop 0
	global_load_lds_dwordx4 v204, s[8:9]
	s_cbranch_scc1 .LBB0_920
	s_barrier
.LBB0_920:
	s_lshl_b32 s73, s18, 8
	s_lshl_b32 s36, s2, 8
	s_add_u32 s18, s90, 0x1c000000
	s_addc_u32 s19, s91, 0
	s_and_b32 s21, s21, 3
	s_lshl_b32 s61, s22, 6
	s_lshl_b32 s22, s22, 13
	s_lshl_b32 s23, s21, 12
	s_add_u32 s2, s44, 0x80000
	s_addc_u32 s3, s45, 0
	s_add_i32 m0, s53, 0x18000
	v_lshl_add_u64 v[4:5], s[2:3], 0, v[198:199]
	s_waitcnt vmcnt(2)
	s_barrier
	global_load_lds_dwordx4 v[4:5], off
	s_add_i32 m0, s53, 0x1a000
	v_lshl_add_u64 v[4:5], s[2:3], 0, v[200:201]
	s_add_u32 s2, s90, 0x6000080
	s_addc_u32 s3, s91, 0
	s_add_i32 s62, s53, 0x8000
	global_load_lds_dwordx4 v[4:5], off
	v_lshl_add_u64 v[4:5], s[2:3], 0, v[196:197]
	s_mov_b32 m0, s62
	s_add_i32 s63, s53, 0xa000
	global_load_lds_dwordx4 v[4:5], off
	v_lshl_add_u64 v[4:5], s[2:3], 0, v[202:203]
	s_add_u32 s2, s44, 0x80400
	s_mov_b32 m0, s63
	s_addc_u32 s3, s45, 0
	global_load_lds_dwordx4 v[4:5], off
	s_add_i32 m0, s53, 0x1c000
	v_lshl_add_u64 v[4:5], s[2:3], 0, v[198:199]
	global_load_lds_dwordx4 v[4:5], off
	v_lshl_add_u64 v[4:5], s[2:3], 0, v[200:201]
	s_add_i32 m0, s53, 0x1e000
	s_movk_i32 s2, 0x3c0
	global_load_lds_dwordx4 v[4:5], off
	v_lshlrev_b32_e32 v4, 6, v0
	v_and_or_b32 v2, v4, s2, v2
	s_lshl_b32 s2, s21, 8
	v_lshlrev_b32_e32 v4, 2, v0
	s_add_i32 s66, s2, 0
	v_and_b32_e32 v4, 32, v4
	s_lshl_b32 s64, s21, 6
	s_add_i32 s65, s66, 0x22800
	v_bitop3_b32 v212, s23, v2, v4 bitop3:0xf6
	s_waitcnt vmcnt(6)
	s_cmpk_lt_u32 s20, 0x100
	v_bitop3_b32 v5, v2, s22, v4 bitop3:0xde
	s_cselect_b64 s[20:21], -1, 0
	s_add_i32 s2, 0, 0x22000
	v_add_u32_e32 v2, 0, v212
	s_add_i32 s66, s66, 0x23400
	v_mov_b32_e32 v213, s2
	s_lshl_b32 s67, s64, 2
	v_lshlrev_b32_e32 v214, 2, v194
	v_add_u32_e32 v215, 0x10000, v2
	v_add_u32_e32 v216, 0x14000, v2
	v_add_u32_e32 v217, 0, v5
	s_mov_b64 s[22:23], 0x80
	v_mov_b32_e32 v218, 0x7f7f7f7f
	s_movk_i32 s68, 0x80
	s_mov_b32 s24, 0x3c800000
	s_mov_b32 s69, 0xc0e00000
	v_mov_b32_e32 v219, 0x40e00000
	v_mov_b32_e32 v206, v196
	v_mov_b32_e32 v196, v3
	s_mov_b64 s[38:39], s[8:9]
	s_barrier
	s_branch .LBB0_923

; template <class Epi, class Sched, bool GATHER, bool FP8>
; __device__ __forceinline__ void gemm_phase(LAS uchar* lds, const int K, const int LDA, const int LDB, const size_t kstepA, const size_t kstepB, const Sched& S, const Epi& E) {
;     ...
;         const bool has_next = S.next(ui + 1, nxt);
;         if constexpr (GATHER) { if (has_next) S.prefetch(nxt, lds + LDS_IDX + ((ui + 1) & 1) * 1024, wid, lane); }
;         E.prefetch(cur, lds + LDS_BIAS + (ui & 1) * 1024, wid, lane);
;         const char* nA = has_next ? nxt.pa : cA; const char* nB = has_next ? nxt.pb : cB;
;     __device__ __forceinline__ bool next(int i, pg8::Unit& u) const {
;         const int NB = __builtin_amdgcn_readfirstlane(tab[0]); const int L = i * G + c; if (L >= NB * nN) return false;
;         const int b = L / nN, pn = L - b * nN, e = __builtin_amdgcn_readfirstlane(tab[64 + b]);
;         u.pa = A; u.pb = B + (size_t)e * bexp + (size_t)pn * 256 * 128; u.row0 = b * 256; u.col0 = pn * 256; u.aux = e; u.blk = b; return true;
.LBB0_923:
	ds_read_b32 v2, v213
	s_add_i32 s71, s46, 1
	s_mul_i32 s2, s71, s92
	s_add_i32 s2, s2, s98
	s_waitcnt lgkmcnt(0)
	v_readfirstlane_b32 s3, v2
	s_lshl_b32 s3, s3, 4
	s_cmp_lt_i32 s2, s3
	s_cselect_b64 s[40:41], -1, 0
	s_cmp_ge_i32 s2, s3
	s_cbranch_scc1 .LBB0_925
	s_ashr_i32 s3, s2, 31
	s_lshr_b32 s3, s3, 28
	s_add_i32 s3, s2, s3
	s_ashr_i32 s70, s3, 4
	s_lshl_b32 s26, s70, 2
	s_add_i32 s26, s26, 0
	s_add_i32 s26, s26, 0x22100
	v_mov_b32_e32 v2, s26
	ds_read_b32 v2, v2
	s_and_b32 s3, s3, -16
	s_sub_i32 s2, s2, s3
	s_waitcnt lgkmcnt(0)
	v_readfirstlane_b32 s26, v2
	s_ashr_i32 s27, s26, 31
	s_lshl_b64 s[28:29], s[26:27], 23
	s_add_u32 s27, s25, s28
	s_addc_u32 s30, s33, s29
	s_ashr_i32 s3, s2, 31
	s_lshl_b64 s[28:29], s[2:3], 15
	s_add_u32 s28, s27, s28
	s_addc_u32 s29, s30, s29
	s_lshl_b32 s72, s70, 8
	s_lshl_b32 s27, s2, 8

; #define LAS __attribute__((address_space(3)))
; #define EPI_LANE() int tz = threadIdx.x; asm volatile("" : "+v"(tz)); const int fr = tz & 15, fq = (tz >> 4) & 3; (void)fr_; (void)fq_
;     __device__ __forceinline__ void operator()(const f32x4 (&acc)[2][2][4][2], const pg8::Unit& u, int wr, int wc, int fr_, int fq_, const LAS uchar* bl) const {
;         EPI_LANE();
;         const int row0 = u.row0 + wr * 64 + fr, col0 = u.col0 + wc * 64 + 16 * fq;
;         const LAS float* bp = (const LAS float*)bl + wc * 64 + 16 * fq;
;         f32x4 bg[2], bu[2];
; #pragma unroll
;         for (int bj = 0; bj < 2; ++bj) { const f32x4 b0 = *(const LAS f32x4*)(bp + bj * 8), b1 = *(const LAS f32x4*)(bp + bj * 8 + 4);
;             bg[bj] = (f32x4){b0.x, b0.z, b1.x, b1.z}; bu[bj] = (f32x4){b0.y, b0.w, b1.y, b1.w}; }
; #pragma unroll
;         for (int ai = 0; ai < 2; ++ai)
; #pragma unroll
;             for (int m = 0; m < 4; ++m) { uchar* rowp = ACT + (size_t)(row0 + ai * 128 + m * 16) * W8LD + (col0 >> 1);
;                 u32x2 w;
; #pragma unroll
;                 for (int bj = 0; bj < 2; ++bj) { f32x4 g = acc[ai][bj][m][0] * W8_INV + bg[bj], up = acc[ai][bj][m][1] * W8_INV + bu[bj];
; #pragma unroll
;                     for (int j = 0; j < 4; ++j) { g[j] = fminf(g[j], 7.f); up[j] = fminf(fmaxf(up[j], -7.f), 7.f); }
;                     const f32x4 a = g * (-1.702f * 1.44269504f);
;                     f32x4 d;
; #pragma unroll
;                     for (int j = 0; j < 4; ++j) d[j] = __builtin_amdgcn_exp2f(a[j]);
;                     d = d + 1.f;
; #pragma unroll
;                     for (int j = 0; j < 4; ++j) d[j] = __builtin_amdgcn_rcpf(d[j]);
;                     const f32x4 o = (up + 1.f) * (g * d);
;                     const unsigned p = pk_fp8x4_nc(o[0], o[1], o[2], o[3]);
;                     if (bj == 0) w.x = p; else w.y = p; }
;                 *(u32x2*)rowp = w; }
.LBB0_933:
	v_mov_b32_e32 v18, v0
	s_add_i32 s38, s73, s61
	v_and_b32_e32 v19, 48, v18
	v_lshl_add_u32 v6, v19, 2, s37
	ds_read_b128 v[10:13], v6
	ds_read_b128 v[14:17], v6 offset:16
	ds_read_b128 v[2:5], v6 offset:32
	ds_read_b128 v[6:9], v6 offset:48
	s_add_i32 s36, s36, s64
	s_waitcnt lgkmcnt(0)
	v_mov_b32_e32 v24, v10
	v_mov_b32_e32 v22, v14
	v_mov_b32_e32 v23, v16
	v_mov_b32_e32 v25, v12
	v_pk_fma_f32 v[28:29], v[192:193], s[24:25], v[22:23] op_sel_hi:[1,0,1]
	v_pk_fma_f32 v[30:31], v[190:191], s[24:25], v[24:25] op_sel_hi:[1,0,1]
	v_min_f32_e32 v28, 0x40e00000, v28
	v_min_f32_e32 v30, 0x40e00000, v30
	v_min_f32_e32 v31, 0x40e00000, v31
	v_min_f32_e32 v29, 0x40e00000, v29
	v_mul_f32_e32 v27, 0xc01d265f, v30
	v_mul_f32_e32 v33, 0xc01d265f, v28
	v_exp_f32_e32 v32, v27
	v_mul_f32_e32 v27, 0xc01d265f, v31
	v_exp_f32_e32 v34, v33
	v_mul_f32_e32 v33, 0xc01d265f, v29
	v_exp_f32_e32 v35, v33
	v_exp_f32_e32 v33, v27
	v_mov_b32_e32 v12, v11
	v_pk_fma_f32 v[10:11], v[186:187], s[24:25], v[12:13] op_sel_hi:[1,0,1]
	v_pk_add_f32 v[34:35], v[34:35], 1.0 op_sel_hi:[1,0]
	v_pk_add_f32 v[32:33], v[32:33], 1.0 op_sel_hi:[1,0]
	v_rcp_f32_e32 v34, v34
	v_rcp_f32_e32 v32, v32
	v_rcp_f32_e32 v33, v33
	v_rcp_f32_e32 v35, v35
	v_mov_b32_e32 v16, v15
	v_med3_f32 v10, v10, s69, v219
	v_med3_f32 v11, v11, s69, v219
	v_pk_fma_f32 v[14:15], v[188:189], s[24:25], v[16:17] op_sel_hi:[1,0,1]
	v_pk_add_f32 v[10:11], v[10:11], 1.0 op_sel_hi:[1,0]
	v_pk_mul_f32 v[30:31], v[30:31], v[32:33]
	v_med3_f32 v14, v14, s69, v219
	v_med3_f32 v15, v15, s69, v219
	v_pk_mul_f32 v[10:11], v[10:11], v[30:31]
	v_mov_b32_e32 v30, v197
	v_cvt_pk_fp8_f32 v30, v10, v11
	v_pk_add_f32 v[10:11], v[14:15], 1.0 op_sel_hi:[1,0]
	v_pk_mul_f32 v[14:15], v[28:29], v[34:35]
	v_and_b32_e32 v18, 15, v18
	v_pk_mul_f32 v[10:11], v[10:11], v[14:15]
	v_mov_b32_e32 v14, v2
	v_mov_b32_e32 v15, v4
	v_pk_fma_f32 v[32:33], v[182:183], s[24:25], v[14:15] op_sel_hi:[1,0,1]
	v_cvt_pk_fp8_f32 v30, v10, v11 op_sel:[0,0,1]
	v_min_f32_e32 v32, 0x40e00000, v32
	v_min_f32_e32 v33, 0x40e00000, v33
	v_mul_f32_e32 v27, 0xc01d265f, v32
	v_mov_b32_e32 v10, v6
	v_mov_b32_e32 v11, v8
	v_exp_f32_e32 v34, v27
	v_mul_f32_e32 v27, 0xc01d265f, v33
	v_pk_fma_f32 v[28:29], v[184:185], s[24:25], v[10:11] op_sel_hi:[1,0,1]
	v_exp_f32_e32 v35, v27
	v_min_f32_e32 v28, 0x40e00000, v28
	v_min_f32_e32 v29, 0x40e00000, v29
	v_mul_f32_e32 v31, 0xc01d265f, v28
	v_exp_f32_e32 v36, v31
	v_mul_f32_e32 v31, 0xc01d265f, v29
	v_exp_f32_e32 v37, v31
	v_pk_add_f32 v[34:35], v[34:35], 1.0 op_sel_hi:[1,0]
	v_mov_b32_e32 v4, v3
	v_rcp_f32_e32 v34, v34
	v_rcp_f32_e32 v35, v35
	v_pk_fma_f32 v[2:3], v[178:179], s[24:25], v[4:5] op_sel_hi:[1,0,1]
	v_pk_add_f32 v[36:37], v[36:37], 1.0 op_sel_hi:[1,0]
	v_med3_f32 v2, v2, s69, v219
	v_med3_f32 v3, v3, s69, v219
	v_rcp_f32_e32 v36, v36
	v_rcp_f32_e32 v37, v37
	v_pk_add_f32 v[2:3], v[2:3], 1.0 op_sel_hi:[1,0]
	v_pk_mul_f32 v[32:33], v[32:33], v[34:35]
	v_mov_b32_e32 v8, v7
	v_pk_mul_f32 v[2:3], v[2:3], v[32:33]
	v_mov_b32_e32 v31, v197
	v_pk_fma_f32 v[6:7], v[180:181], s[24:25], v[8:9] op_sel_hi:[1,0,1]
	v_cvt_pk_fp8_f32 v31, v2, v3
	v_med3_f32 v6, v6, s69, v219
	v_med3_f32 v7, v7, s69, v219
	v_pk_add_f32 v[2:3], v[6:7], 1.0 op_sel_hi:[1,0]
	v_pk_mul_f32 v[6:7], v[28:29], v[36:37]
	v_add_u32_e32 v26, s38, v18
	v_pk_mul_f32 v[2:3], v[2:3], v[6:7]
	v_add_u32_e32 v18, s36, v19
	v_cvt_pk_fp8_f32 v31, v2, v3 op_sel:[0,0,1]
	v_pk_fma_f32 v[6:7], v[174:175], s[24:25], v[24:25] op_sel_hi:[1,0,1]
	v_ashrrev_i32_e32 v18, 1, v18
	s_mov_b32 s100, 0x4fff80
	v_lshrrev_b32_e32 v249, 7, v18
	v_mad_u32_u24 v18, v249, s100, v18
	v_mov_b64_e32 v[20:21], s[18:19]
	v_min_f32_e32 v6, 0x40e00000, v6
	v_min_f32_e32 v7, 0x40e00000, v7
	v_ashrrev_i32_e32 v19, 31, v18
	v_mad_i64_i32 v[2:3], s[36:37], v26, s68, v[20:21]
	v_mul_f32_e32 v32, 0xc01d265f, v6
	v_mul_f32_e32 v33, 0xc01d265f, v7
	v_lshl_add_u64 v[2:3], v[2:3], 0, v[18:19]
	v_exp_f32_e32 v32, v32
	v_exp_f32_e32 v33, v33
	global_store_dwordx2 v[2:3], v[30:31], off
	v_pk_fma_f32 v[2:3], v[176:177], s[24:25], v[22:23] op_sel_hi:[1,0,1]
	v_pk_fma_f32 v[30:31], v[170:171], s[24:25], v[12:13] op_sel_hi:[1,0,1]
	v_min_f32_e32 v2, 0x40e00000, v2
	v_min_f32_e32 v3, 0x40e00000, v3
	v_mul_f32_e32 v34, 0xc01d265f, v2
	v_mul_f32_e32 v35, 0xc01d265f, v3
	v_exp_f32_e32 v34, v34
	v_exp_f32_e32 v35, v35
	v_pk_add_f32 v[32:33], v[32:33], 1.0 op_sel_hi:[1,0]
	v_med3_f32 v30, v30, s69, v219
	v_rcp_f32_e32 v32, v32
	v_rcp_f32_e32 v33, v33
	v_med3_f32 v31, v31, s69, v219
	v_pk_add_f32 v[34:35], v[34:35], 1.0 op_sel_hi:[1,0]
	v_pk_add_f32 v[30:31], v[30:31], 1.0 op_sel_hi:[1,0]
	v_rcp_f32_e32 v34, v34
	v_rcp_f32_e32 v35, v35
	v_pk_mul_f32 v[6:7], v[6:7], v[32:33]
	v_pk_fma_f32 v[28:29], v[172:173], s[24:25], v[16:17] op_sel_hi:[1,0,1]
	v_pk_mul_f32 v[6:7], v[30:31], v[6:7]
	v_mov_b32_e32 v30, v197
	v_cvt_pk_fp8_f32 v30, v6, v7
	v_med3_f32 v28, v28, s69, v219
	v_med3_f32 v29, v29, s69, v219
	v_pk_add_f32 v[6:7], v[28:29], 1.0 op_sel_hi:[1,0]
	v_pk_mul_f32 v[2:3], v[2:3], v[34:35]
	v_pk_fma_f32 v[32:33], v[162:163], s[24:25], v[4:5] op_sel_hi:[1,0,1]
	v_pk_mul_f32 v[2:3], v[6:7], v[2:3]
	v_pk_fma_f32 v[6:7], v[166:167], s[24:25], v[14:15] op_sel_hi:[1,0,1]
	v_cvt_pk_fp8_f32 v30, v2, v3 op_sel:[0,0,1]
	v_pk_fma_f32 v[2:3], v[168:169], s[24:25], v[10:11] op_sel_hi:[1,0,1]
	v_min_f32_e32 v6, 0x40e00000, v6
	v_min_f32_e32 v2, 0x40e00000, v2
	v_min_f32_e32 v7, 0x40e00000, v7
	v_min_f32_e32 v3, 0x40e00000, v3
	v_mul_f32_e32 v31, 0xc01d265f, v6
	v_mul_f32_e32 v35, 0xc01d265f, v2
	v_exp_f32_e32 v34, v31
	v_mul_f32_e32 v31, 0xc01d265f, v7
	v_exp_f32_e32 v36, v35
	v_mul_f32_e32 v35, 0xc01d265f, v3
;     __device__ __forceinline__ void operator()(const f32x4 (&acc)[2][2][4][2], const pg8::Unit& u, int wr, int wc, int fr_, int fq_, const LAS uchar* bl) const {
;     ...
; #pragma unroll
;         for (int ai = 0; ai < 2; ++ai)
; #pragma unroll
;             for (int m = 0; m < 4; ++m) { uchar* rowp = ACT + (size_t)(row0 + ai * 128 + m * 16) * W8LD + (col0 >> 1);
;                 u32x2 w;
; #pragma unroll
;                 for (int bj = 0; bj < 2; ++bj) { f32x4 g = acc[ai][bj][m][0] * W8_INV + bg[bj], up = acc[ai][bj][m][1] * W8_INV + bu[bj];
; #pragma unroll
;                     for (int j = 0; j < 4; ++j) { g[j] = fminf(g[j], 7.f); up[j] = fminf(fmaxf(up[j], -7.f), 7.f); }
;                     const f32x4 a = g * (-1.702f * 1.44269504f);
;                     f32x4 d;
; #pragma unroll
;                     for (int j = 0; j < 4; ++j) d[j] = __builtin_amdgcn_exp2f(a[j]);
;                     d = d + 1.f;
; #pragma unroll
;                     for (int j = 0; j < 4; ++j) d[j] = __builtin_amdgcn_rcpf(d[j]);
;                     const f32x4 o = (up + 1.f) * (g * d);
;                     const unsigned p = pk_fp8x4_nc(o[0], o[1], o[2], o[3]);
;                     if (bj == 0) w.x = p; else w.y = p; }
;                 *(u32x2*)rowp = w; }
	v_exp_f32_e32 v37, v35
	v_exp_f32_e32 v35, v31
	v_med3_f32 v32, v32, s69, v219
	v_med3_f32 v33, v33, s69, v219
	v_pk_add_f32 v[36:37], v[36:37], 1.0 op_sel_hi:[1,0]
	v_pk_add_f32 v[34:35], v[34:35], 1.0 op_sel_hi:[1,0]
	v_rcp_f32_e32 v36, v36
	v_rcp_f32_e32 v34, v34
	v_rcp_f32_e32 v35, v35
	v_rcp_f32_e32 v37, v37
	v_pk_add_f32 v[32:33], v[32:33], 1.0 op_sel_hi:[1,0]
	v_mov_b32_e32 v31, v197
	v_pk_mul_f32 v[6:7], v[6:7], v[34:35]
	v_pk_fma_f32 v[28:29], v[164:165], s[24:25], v[8:9] op_sel_hi:[1,0,1]
	v_pk_mul_f32 v[6:7], v[32:33], v[6:7]
	v_med3_f32 v28, v28, s69, v219
	v_cvt_pk_fp8_f32 v31, v6, v7
	v_med3_f32 v29, v29, s69, v219
	v_pk_add_f32 v[6:7], v[28:29], 1.0 op_sel_hi:[1,0]
	v_pk_mul_f32 v[2:3], v[2:3], v[36:37]
	v_add_u32_e32 v27, 16, v26
	v_pk_mul_f32 v[2:3], v[6:7], v[2:3]
	v_pk_fma_f32 v[6:7], v[158:159], s[24:25], v[24:25] op_sel_hi:[1,0,1]
	v_cvt_pk_fp8_f32 v31, v2, v3 op_sel:[0,0,1]
	v_min_f32_e32 v6, 0x40e00000, v6
	v_min_f32_e32 v7, 0x40e00000, v7
	v_mad_i64_i32 v[2:3], s[36:37], v27, s68, v[20:21]
	v_mul_f32_e32 v32, 0xc01d265f, v6
	v_mul_f32_e32 v33, 0xc01d265f, v7
	v_lshl_add_u64 v[2:3], v[2:3], 0, v[18:19]
	v_exp_f32_e32 v32, v32
	v_exp_f32_e32 v33, v33
	global_store_dwordx2 v[2:3], v[30:31], off
	v_pk_fma_f32 v[2:3], v[160:161], s[24:25], v[22:23] op_sel_hi:[1,0,1]
	v_pk_fma_f32 v[30:31], v[154:155], s[24:25], v[12:13] op_sel_hi:[1,0,1]
	v_min_f32_e32 v2, 0x40e00000, v2
	v_min_f32_e32 v3, 0x40e00000, v3
	v_mul_f32_e32 v34, 0xc01d265f, v2
	v_mul_f32_e32 v35, 0xc01d265f, v3
	v_exp_f32_e32 v34, v34
	v_exp_f32_e32 v35, v35
	v_pk_add_f32 v[32:33], v[32:33], 1.0 op_sel_hi:[1,0]
	v_med3_f32 v30, v30, s69, v219
	v_rcp_f32_e32 v32, v32
	v_rcp_f32_e32 v33, v33
	v_med3_f32 v31, v31, s69, v219
	v_pk_add_f32 v[34:35], v[34:35], 1.0 op_sel_hi:[1,0]
	v_pk_add_f32 v[30:31], v[30:31], 1.0 op_sel_hi:[1,0]
	v_rcp_f32_e32 v34, v34
	v_rcp_f32_e32 v35, v35
	v_pk_mul_f32 v[6:7], v[6:7], v[32:33]
	v_pk_fma_f32 v[28:29], v[156:157], s[24:25], v[16:17] op_sel_hi:[1,0,1]
	v_pk_mul_f32 v[6:7], v[30:31], v[6:7]
	v_mov_b32_e32 v30, v197
	v_cvt_pk_fp8_f32 v30, v6, v7
	v_med3_f32 v28, v28, s69, v219
	v_med3_f32 v29, v29, s69, v219
	v_pk_add_f32 v[6:7], v[28:29], 1.0 op_sel_hi:[1,0]
	v_pk_mul_f32 v[2:3], v[2:3], v[34:35]
	v_pk_fma_f32 v[32:33], v[146:147], s[24:25], v[4:5] op_sel_hi:[1,0,1]
	v_pk_mul_f32 v[2:3], v[6:7], v[2:3]
	v_pk_fma_f32 v[6:7], v[150:151], s[24:25], v[14:15] op_sel_hi:[1,0,1]
	v_cvt_pk_fp8_f32 v30, v2, v3 op_sel:[0,0,1]
	v_pk_fma_f32 v[2:3], v[152:153], s[24:25], v[10:11] op_sel_hi:[1,0,1]
	v_min_f32_e32 v6, 0x40e00000, v6
	v_min_f32_e32 v2, 0x40e00000, v2
	v_min_f32_e32 v7, 0x40e00000, v7
	v_min_f32_e32 v3, 0x40e00000, v3
	v_mul_f32_e32 v31, 0xc01d265f, v6
	v_mul_f32_e32 v35, 0xc01d265f, v2
	v_exp_f32_e32 v34, v31
	v_mul_f32_e32 v31, 0xc01d265f, v7
	v_exp_f32_e32 v36, v35
	v_mul_f32_e32 v35, 0xc01d265f, v3
	v_exp_f32_e32 v37, v35
	v_exp_f32_e32 v35, v31
	v_med3_f32 v32, v32, s69, v219
	v_med3_f32 v33, v33, s69, v219
	v_pk_add_f32 v[36:37], v[36:37], 1.0 op_sel_hi:[1,0]
	v_pk_add_f32 v[34:35], v[34:35], 1.0 op_sel_hi:[1,0]
	v_rcp_f32_e32 v36, v36
	v_rcp_f32_e32 v34, v34
	v_rcp_f32_e32 v35, v35
	v_rcp_f32_e32 v37, v37
	v_pk_add_f32 v[32:33], v[32:33], 1.0 op_sel_hi:[1,0]
	v_mov_b32_e32 v31, v197
	v_pk_mul_f32 v[6:7], v[6:7], v[34:35]
	v_pk_fma_f32 v[28:29], v[148:149], s[24:25], v[8:9] op_sel_hi:[1,0,1]
	v_pk_mul_f32 v[6:7], v[32:33], v[6:7]
	v_med3_f32 v28, v28, s69, v219
	v_cvt_pk_fp8_f32 v31, v6, v7
	v_med3_f32 v29, v29, s69, v219
	v_pk_add_f32 v[6:7], v[28:29], 1.0 op_sel_hi:[1,0]
	v_pk_mul_f32 v[2:3], v[2:3], v[36:37]
	v_add_u32_e32 v27, 32, v26
	v_pk_mul_f32 v[2:3], v[6:7], v[2:3]
	v_pk_fma_f32 v[6:7], v[142:143], s[24:25], v[24:25] op_sel_hi:[1,0,1]
	v_cvt_pk_fp8_f32 v31, v2, v3 op_sel:[0,0,1]
	v_min_f32_e32 v6, 0x40e00000, v6
	v_min_f32_e32 v7, 0x40e00000, v7
	v_mad_i64_i32 v[2:3], s[36:37], v27, s68, v[20:21]
	v_mul_f32_e32 v32, 0xc01d265f, v6
	v_mul_f32_e32 v33, 0xc01d265f, v7
	v_lshl_add_u64 v[2:3], v[2:3], 0, v[18:19]
	v_exp_f32_e32 v32, v32
	v_exp_f32_e32 v33, v33
	global_store_dwordx2 v[2:3], v[30:31], off
	v_pk_fma_f32 v[2:3], v[144:145], s[24:25], v[22:23] op_sel_hi:[1,0,1]
	v_pk_fma_f32 v[30:31], v[138:139], s[24:25], v[12:13] op_sel_hi:[1,0,1]
	v_min_f32_e32 v2, 0x40e00000, v2
	v_min_f32_e32 v3, 0x40e00000, v3
	v_mul_f32_e32 v34, 0xc01d265f, v2
	v_mul_f32_e32 v35, 0xc01d265f, v3
	v_exp_f32_e32 v34, v34
	v_exp_f32_e32 v35, v35
	v_pk_add_f32 v[32:33], v[32:33], 1.0 op_sel_hi:[1,0]
	v_med3_f32 v30, v30, s69, v219
	v_rcp_f32_e32 v32, v32
	v_rcp_f32_e32 v33, v33
	v_med3_f32 v31, v31, s69, v219
	v_pk_add_f32 v[34:35], v[34:35], 1.0 op_sel_hi:[1,0]
	v_pk_add_f32 v[30:31], v[30:31], 1.0 op_sel_hi:[1,0]
	v_rcp_f32_e32 v34, v34
	v_rcp_f32_e32 v35, v35
	v_pk_mul_f32 v[6:7], v[6:7], v[32:33]
	v_pk_fma_f32 v[28:29], v[140:141], s[24:25], v[16:17] op_sel_hi:[1,0,1]
	v_pk_mul_f32 v[6:7], v[30:31], v[6:7]
	v_mov_b32_e32 v30, v197
	v_cvt_pk_fp8_f32 v30, v6, v7
	v_med3_f32 v28, v28, s69, v219
	v_med3_f32 v29, v29, s69, v219
	v_pk_add_f32 v[6:7], v[28:29], 1.0 op_sel_hi:[1,0]
	v_pk_mul_f32 v[2:3], v[2:3], v[34:35]
	v_pk_fma_f32 v[32:33], v[130:131], s[24:25], v[4:5] op_sel_hi:[1,0,1]
	v_pk_mul_f32 v[2:3], v[6:7], v[2:3]
	v_pk_fma_f32 v[6:7], v[134:135], s[24:25], v[14:15] op_sel_hi:[1,0,1]
	v_cvt_pk_fp8_f32 v30, v2, v3 op_sel:[0,0,1]
	v_pk_fma_f32 v[2:3], v[136:137], s[24:25], v[10:11] op_sel_hi:[1,0,1]
	v_min_f32_e32 v6, 0x40e00000, v6
	v_min_f32_e32 v2, 0x40e00000, v2
	v_min_f32_e32 v7, 0x40e00000, v7
	v_min_f32_e32 v3, 0x40e00000, v3
	v_mul_f32_e32 v31, 0xc01d265f, v6
	v_mul_f32_e32 v35, 0xc01d265f, v2
	v_exp_f32_e32 v34, v31
;     __device__ __forceinline__ void operator()(const f32x4 (&acc)[2][2][4][2], const pg8::Unit& u, int wr, int wc, int fr_, int fq_, const LAS uchar* bl) const {
;     ...
; #pragma unroll
;         for (int ai = 0; ai < 2; ++ai)
; #pragma unroll
;             for (int m = 0; m < 4; ++m) { uchar* rowp = ACT + (size_t)(row0 + ai * 128 + m * 16) * W8LD + (col0 >> 1);
;                 u32x2 w;
; #pragma unroll
;                 for (int bj = 0; bj < 2; ++bj) { f32x4 g = acc[ai][bj][m][0] * W8_INV + bg[bj], up = acc[ai][bj][m][1] * W8_INV + bu[bj];
; #pragma unroll
;                     for (int j = 0; j < 4; ++j) { g[j] = fminf(g[j], 7.f); up[j] = fminf(fmaxf(up[j], -7.f), 7.f); }
;                     const f32x4 a = g * (-1.702f * 1.44269504f);
;                     f32x4 d;
; #pragma unroll
;                     for (int j = 0; j < 4; ++j) d[j] = __builtin_amdgcn_exp2f(a[j]);
;                     d = d + 1.f;
; #pragma unroll
;                     for (int j = 0; j < 4; ++j) d[j] = __builtin_amdgcn_rcpf(d[j]);
;                     const f32x4 o = (up + 1.f) * (g * d);
;                     const unsigned p = pk_fp8x4_nc(o[0], o[1], o[2], o[3]);
;                     if (bj == 0) w.x = p; else w.y = p; }
;                 *(u32x2*)rowp = w; }
	v_mul_f32_e32 v31, 0xc01d265f, v7
	v_exp_f32_e32 v36, v35
	v_mul_f32_e32 v35, 0xc01d265f, v3
	v_exp_f32_e32 v37, v35
	v_exp_f32_e32 v35, v31
	v_med3_f32 v32, v32, s69, v219
	v_med3_f32 v33, v33, s69, v219
	v_pk_add_f32 v[36:37], v[36:37], 1.0 op_sel_hi:[1,0]
	v_pk_add_f32 v[34:35], v[34:35], 1.0 op_sel_hi:[1,0]
	v_rcp_f32_e32 v36, v36
	v_rcp_f32_e32 v34, v34
	v_rcp_f32_e32 v35, v35
	v_rcp_f32_e32 v37, v37
	v_pk_add_f32 v[32:33], v[32:33], 1.0 op_sel_hi:[1,0]
	v_mov_b32_e32 v31, v197
	v_pk_mul_f32 v[6:7], v[6:7], v[34:35]
	v_pk_fma_f32 v[28:29], v[132:133], s[24:25], v[8:9] op_sel_hi:[1,0,1]
	v_pk_mul_f32 v[6:7], v[32:33], v[6:7]
	v_med3_f32 v28, v28, s69, v219
	v_cvt_pk_fp8_f32 v31, v6, v7
	v_med3_f32 v29, v29, s69, v219
	v_pk_add_f32 v[6:7], v[28:29], 1.0 op_sel_hi:[1,0]
	v_pk_mul_f32 v[2:3], v[2:3], v[36:37]
	v_add_u32_e32 v27, 48, v26
	v_pk_mul_f32 v[2:3], v[6:7], v[2:3]
	v_pk_fma_f32 v[6:7], v[126:127], s[24:25], v[24:25] op_sel_hi:[1,0,1]
	v_cvt_pk_fp8_f32 v31, v2, v3 op_sel:[0,0,1]
	v_min_f32_e32 v6, 0x40e00000, v6
	v_min_f32_e32 v7, 0x40e00000, v7
	v_mad_i64_i32 v[2:3], s[36:37], v27, s68, v[20:21]
	v_mul_f32_e32 v32, 0xc01d265f, v6
	v_mul_f32_e32 v33, 0xc01d265f, v7
	v_lshl_add_u64 v[2:3], v[2:3], 0, v[18:19]
	v_exp_f32_e32 v32, v32
	v_exp_f32_e32 v33, v33
	global_store_dwordx2 v[2:3], v[30:31], off
	v_pk_fma_f32 v[2:3], v[128:129], s[24:25], v[22:23] op_sel_hi:[1,0,1]
	v_pk_fma_f32 v[30:31], v[122:123], s[24:25], v[12:13] op_sel_hi:[1,0,1]
	v_min_f32_e32 v2, 0x40e00000, v2
	v_min_f32_e32 v3, 0x40e00000, v3
	v_mul_f32_e32 v34, 0xc01d265f, v2
	v_mul_f32_e32 v35, 0xc01d265f, v3
	v_exp_f32_e32 v34, v34
	v_exp_f32_e32 v35, v35
	v_pk_add_f32 v[32:33], v[32:33], 1.0 op_sel_hi:[1,0]
	v_med3_f32 v30, v30, s69, v219
	v_rcp_f32_e32 v32, v32
	v_rcp_f32_e32 v33, v33
	v_med3_f32 v31, v31, s69, v219
	v_pk_add_f32 v[34:35], v[34:35], 1.0 op_sel_hi:[1,0]
	v_pk_add_f32 v[30:31], v[30:31], 1.0 op_sel_hi:[1,0]
	v_rcp_f32_e32 v34, v34
	v_rcp_f32_e32 v35, v35
	v_pk_mul_f32 v[6:7], v[6:7], v[32:33]
	v_pk_fma_f32 v[28:29], v[124:125], s[24:25], v[16:17] op_sel_hi:[1,0,1]
	v_pk_mul_f32 v[6:7], v[30:31], v[6:7]
	v_mov_b32_e32 v30, v197
	v_cvt_pk_fp8_f32 v30, v6, v7
	v_med3_f32 v28, v28, s69, v219
	v_med3_f32 v29, v29, s69, v219
	v_pk_add_f32 v[6:7], v[28:29], 1.0 op_sel_hi:[1,0]
	v_pk_mul_f32 v[2:3], v[2:3], v[34:35]
	v_pk_fma_f32 v[32:33], v[114:115], s[24:25], v[4:5] op_sel_hi:[1,0,1]
	v_pk_mul_f32 v[2:3], v[6:7], v[2:3]
	v_pk_fma_f32 v[6:7], v[118:119], s[24:25], v[14:15] op_sel_hi:[1,0,1]
	v_cvt_pk_fp8_f32 v30, v2, v3 op_sel:[0,0,1]
	v_pk_fma_f32 v[2:3], v[120:121], s[24:25], v[10:11] op_sel_hi:[1,0,1]
	v_min_f32_e32 v6, 0x40e00000, v6
	v_min_f32_e32 v2, 0x40e00000, v2
	v_min_f32_e32 v7, 0x40e00000, v7
	v_min_f32_e32 v3, 0x40e00000, v3
	v_mul_f32_e32 v31, 0xc01d265f, v6
	v_mul_f32_e32 v35, 0xc01d265f, v2
	v_exp_f32_e32 v34, v31
	v_mul_f32_e32 v31, 0xc01d265f, v7
	v_exp_f32_e32 v36, v35
	v_mul_f32_e32 v35, 0xc01d265f, v3
	v_exp_f32_e32 v37, v35
	v_exp_f32_e32 v35, v31
	v_med3_f32 v32, v32, s69, v219
	v_med3_f32 v33, v33, s69, v219
	v_pk_add_f32 v[36:37], v[36:37], 1.0 op_sel_hi:[1,0]
	v_pk_add_f32 v[34:35], v[34:35], 1.0 op_sel_hi:[1,0]
	v_rcp_f32_e32 v36, v36
	v_rcp_f32_e32 v34, v34
	v_rcp_f32_e32 v35, v35
	v_rcp_f32_e32 v37, v37
	v_pk_add_f32 v[32:33], v[32:33], 1.0 op_sel_hi:[1,0]
	v_mov_b32_e32 v31, v197
	v_pk_mul_f32 v[6:7], v[6:7], v[34:35]
	v_pk_fma_f32 v[28:29], v[116:117], s[24:25], v[8:9] op_sel_hi:[1,0,1]
	v_pk_mul_f32 v[6:7], v[32:33], v[6:7]
	v_med3_f32 v28, v28, s69, v219
	v_cvt_pk_fp8_f32 v31, v6, v7
	v_med3_f32 v29, v29, s69, v219
	v_pk_add_f32 v[6:7], v[28:29], 1.0 op_sel_hi:[1,0]
	v_pk_mul_f32 v[2:3], v[2:3], v[36:37]
	v_add_u32_e32 v27, 0x80, v26
	v_pk_mul_f32 v[2:3], v[6:7], v[2:3]
	v_pk_fma_f32 v[6:7], v[110:111], s[24:25], v[24:25] op_sel_hi:[1,0,1]
	v_cvt_pk_fp8_f32 v31, v2, v3 op_sel:[0,0,1]
	v_min_f32_e32 v6, 0x40e00000, v6
	v_min_f32_e32 v7, 0x40e00000, v7
	v_mad_i64_i32 v[2:3], s[36:37], v27, s68, v[20:21]
	v_mul_f32_e32 v32, 0xc01d265f, v6
	v_mul_f32_e32 v33, 0xc01d265f, v7
	v_lshl_add_u64 v[2:3], v[2:3], 0, v[18:19]
	v_exp_f32_e32 v32, v32
	v_exp_f32_e32 v33, v33
	global_store_dwordx2 v[2:3], v[30:31], off
	v_pk_fma_f32 v[2:3], v[112:113], s[24:25], v[22:23] op_sel_hi:[1,0,1]
	v_pk_fma_f32 v[30:31], v[106:107], s[24:25], v[12:13] op_sel_hi:[1,0,1]
	v_min_f32_e32 v2, 0x40e00000, v2
	v_min_f32_e32 v3, 0x40e00000, v3
	v_mul_f32_e32 v34, 0xc01d265f, v2
	v_mul_f32_e32 v35, 0xc01d265f, v3
	v_exp_f32_e32 v34, v34
	v_exp_f32_e32 v35, v35
	v_pk_add_f32 v[32:33], v[32:33], 1.0 op_sel_hi:[1,0]
	v_med3_f32 v30, v30, s69, v219
	v_rcp_f32_e32 v32, v32
	v_rcp_f32_e32 v33, v33
	v_med3_f32 v31, v31, s69, v219
	v_pk_add_f32 v[34:35], v[34:35], 1.0 op_sel_hi:[1,0]
	v_pk_add_f32 v[30:31], v[30:31], 1.0 op_sel_hi:[1,0]
	v_rcp_f32_e32 v34, v34
	v_rcp_f32_e32 v35, v35
	v_pk_mul_f32 v[6:7], v[6:7], v[32:33]
	v_pk_fma_f32 v[28:29], v[108:109], s[24:25], v[16:17] op_sel_hi:[1,0,1]
	v_pk_mul_f32 v[6:7], v[30:31], v[6:7]
	v_mov_b32_e32 v30, v197
	v_cvt_pk_fp8_f32 v30, v6, v7
	v_med3_f32 v28, v28, s69, v219
	v_med3_f32 v29, v29, s69, v219
	v_pk_add_f32 v[6:7], v[28:29], 1.0 op_sel_hi:[1,0]
	v_pk_mul_f32 v[2:3], v[2:3], v[34:35]
	v_pk_fma_f32 v[32:33], v[98:99], s[24:25], v[4:5] op_sel_hi:[1,0,1]
	v_pk_mul_f32 v[2:3], v[6:7], v[2:3]
	v_pk_fma_f32 v[6:7], v[102:103], s[24:25], v[14:15] op_sel_hi:[1,0,1]
	v_cvt_pk_fp8_f32 v30, v2, v3 op_sel:[0,0,1]
	v_pk_fma_f32 v[2:3], v[104:105], s[24:25], v[10:11] op_sel_hi:[1,0,1]
	v_min_f32_e32 v6, 0x40e00000, v6
	v_min_f32_e32 v2, 0x40e00000, v2
	v_min_f32_e32 v7, 0x40e00000, v7
	v_min_f32_e32 v3, 0x40e00000, v3
; #define PG8_BAR __builtin_amdgcn_s_barrier()
; template <class Epi, class Sched, bool GATHER, bool FP8>
; __device__ __forceinline__ void gemm_phase(LAS uchar* lds, const int K, const int LDA, const int LDB, const size_t kstepA, const size_t kstepB, const Sched& S, const Epi& E) {
;     ...
;         if (!has_next) break;
; #pragma unroll
;         for (int a = 0; a < 2; ++a)
; #pragma unroll
;             for (int b = 0; b < 2; ++b)
; #pragma unroll
;                 for (int m = 0; m < 4; ++m)
; #pragma unroll
;                     for (int n = 0; n < 2; ++n) acc[a][b][m][n] = (f32x4){0.f, 0.f, 0.f, 0.f};
;         cur = nxt; cA = nA; cB = nB; ++ui;
;         if (wr == 1) PG8_BAR;
;     __device__ __forceinline__ void operator()(const f32x4 (&acc)[2][2][4][2], const pg8::Unit& u, int wr, int wc, int fr_, int fq_, const LAS uchar* bl) const {
;     ...
;         for (int ai = 0; ai < 2; ++ai)
; #pragma unroll
;             for (int m = 0; m < 4; ++m) { uchar* rowp = ACT + (size_t)(row0 + ai * 128 + m * 16) * W8LD + (col0 >> 1);
;                 u32x2 w;
; #pragma unroll
;                 for (int bj = 0; bj < 2; ++bj) { f32x4 g = acc[ai][bj][m][0] * W8_INV + bg[bj], up = acc[ai][bj][m][1] * W8_INV + bu[bj];
; #pragma unroll
;                     for (int j = 0; j < 4; ++j) { g[j] = fminf(g[j], 7.f); up[j] = fminf(fmaxf(up[j], -7.f), 7.f); }
;                     const f32x4 a = g * (-1.702f * 1.44269504f);
;                     f32x4 d;
; #pragma unroll
;                     for (int j = 0; j < 4; ++j) d[j] = __builtin_amdgcn_exp2f(a[j]);
;                     d = d + 1.f;
; #pragma unroll
;                     for (int j = 0; j < 4; ++j) d[j] = __builtin_amdgcn_rcpf(d[j]);
;                     const f32x4 o = (up + 1.f) * (g * d);
;                     const unsigned p = pk_fp8x4_nc(o[0], o[1], o[2], o[3]);
;                     if (bj == 0) w.x = p; else w.y = p; }
;                 *(u32x2*)rowp = w; }
	v_mul_f32_e32 v31, 0xc01d265f, v6
	v_mul_f32_e32 v35, 0xc01d265f, v2
	v_exp_f32_e32 v34, v31
	v_mul_f32_e32 v31, 0xc01d265f, v7
	v_exp_f32_e32 v36, v35
	v_mul_f32_e32 v35, 0xc01d265f, v3
	v_exp_f32_e32 v37, v35
	v_exp_f32_e32 v35, v31
	v_med3_f32 v32, v32, s69, v219
	v_med3_f32 v33, v33, s69, v219
	v_pk_add_f32 v[36:37], v[36:37], 1.0 op_sel_hi:[1,0]
	v_pk_add_f32 v[34:35], v[34:35], 1.0 op_sel_hi:[1,0]
	v_rcp_f32_e32 v36, v36
	v_rcp_f32_e32 v34, v34
	v_rcp_f32_e32 v35, v35
	v_rcp_f32_e32 v37, v37
	v_pk_add_f32 v[32:33], v[32:33], 1.0 op_sel_hi:[1,0]
	v_mov_b32_e32 v31, v197
	v_pk_mul_f32 v[6:7], v[6:7], v[34:35]
	v_pk_fma_f32 v[28:29], v[100:101], s[24:25], v[8:9] op_sel_hi:[1,0,1]
	v_pk_mul_f32 v[6:7], v[32:33], v[6:7]
	v_med3_f32 v28, v28, s69, v219
	v_cvt_pk_fp8_f32 v31, v6, v7
	v_med3_f32 v29, v29, s69, v219
	v_pk_add_f32 v[6:7], v[28:29], 1.0 op_sel_hi:[1,0]
	v_pk_mul_f32 v[2:3], v[2:3], v[36:37]
	v_add_u32_e32 v27, 0x90, v26
	v_pk_mul_f32 v[2:3], v[6:7], v[2:3]
	v_pk_fma_f32 v[6:7], v[94:95], s[24:25], v[24:25] op_sel_hi:[1,0,1]
	v_cvt_pk_fp8_f32 v31, v2, v3 op_sel:[0,0,1]
	v_min_f32_e32 v6, 0x40e00000, v6
	v_min_f32_e32 v7, 0x40e00000, v7
	v_mad_i64_i32 v[2:3], s[36:37], v27, s68, v[20:21]
	v_mul_f32_e32 v32, 0xc01d265f, v6
	v_mul_f32_e32 v33, 0xc01d265f, v7
	v_lshl_add_u64 v[2:3], v[2:3], 0, v[18:19]
	v_exp_f32_e32 v32, v32
	v_exp_f32_e32 v33, v33
	global_store_dwordx2 v[2:3], v[30:31], off
	v_pk_fma_f32 v[2:3], v[96:97], s[24:25], v[22:23] op_sel_hi:[1,0,1]
	v_pk_fma_f32 v[30:31], v[90:91], s[24:25], v[12:13] op_sel_hi:[1,0,1]
	v_min_f32_e32 v2, 0x40e00000, v2
	v_min_f32_e32 v3, 0x40e00000, v3
	v_mul_f32_e32 v34, 0xc01d265f, v2
	v_mul_f32_e32 v35, 0xc01d265f, v3
	v_exp_f32_e32 v34, v34
	v_exp_f32_e32 v35, v35
	v_pk_add_f32 v[32:33], v[32:33], 1.0 op_sel_hi:[1,0]
	v_med3_f32 v30, v30, s69, v219
	v_rcp_f32_e32 v32, v32
	v_rcp_f32_e32 v33, v33
	v_med3_f32 v31, v31, s69, v219
	v_pk_add_f32 v[34:35], v[34:35], 1.0 op_sel_hi:[1,0]
	v_pk_add_f32 v[30:31], v[30:31], 1.0 op_sel_hi:[1,0]
	v_rcp_f32_e32 v34, v34
	v_rcp_f32_e32 v35, v35
	v_pk_mul_f32 v[6:7], v[6:7], v[32:33]
	v_pk_fma_f32 v[28:29], v[92:93], s[24:25], v[16:17] op_sel_hi:[1,0,1]
	v_pk_mul_f32 v[6:7], v[30:31], v[6:7]
	v_mov_b32_e32 v30, v197
	v_cvt_pk_fp8_f32 v30, v6, v7
	v_med3_f32 v28, v28, s69, v219
	v_med3_f32 v29, v29, s69, v219
	v_pk_add_f32 v[6:7], v[28:29], 1.0 op_sel_hi:[1,0]
	v_pk_mul_f32 v[2:3], v[2:3], v[34:35]
	v_pk_fma_f32 v[32:33], v[82:83], s[24:25], v[4:5] op_sel_hi:[1,0,1]
	v_pk_mul_f32 v[2:3], v[6:7], v[2:3]
	v_pk_fma_f32 v[6:7], v[86:87], s[24:25], v[14:15] op_sel_hi:[1,0,1]
	v_cvt_pk_fp8_f32 v30, v2, v3 op_sel:[0,0,1]
	v_pk_fma_f32 v[2:3], v[88:89], s[24:25], v[10:11] op_sel_hi:[1,0,1]
	v_min_f32_e32 v6, 0x40e00000, v6
	v_min_f32_e32 v2, 0x40e00000, v2
	v_min_f32_e32 v7, 0x40e00000, v7
	v_min_f32_e32 v3, 0x40e00000, v3
	v_mul_f32_e32 v31, 0xc01d265f, v6
	v_mul_f32_e32 v35, 0xc01d265f, v2
	v_exp_f32_e32 v34, v31
	v_mul_f32_e32 v31, 0xc01d265f, v7
	v_exp_f32_e32 v36, v35
	v_mul_f32_e32 v35, 0xc01d265f, v3
	v_exp_f32_e32 v37, v35
	v_exp_f32_e32 v35, v31
	v_med3_f32 v32, v32, s69, v219
	v_med3_f32 v33, v33, s69, v219
	v_pk_add_f32 v[36:37], v[36:37], 1.0 op_sel_hi:[1,0]
	v_pk_add_f32 v[34:35], v[34:35], 1.0 op_sel_hi:[1,0]
	v_rcp_f32_e32 v36, v36
	v_rcp_f32_e32 v34, v34
	v_rcp_f32_e32 v35, v35
	v_rcp_f32_e32 v37, v37
	v_pk_add_f32 v[32:33], v[32:33], 1.0 op_sel_hi:[1,0]
	v_mov_b32_e32 v31, v197
	v_pk_mul_f32 v[6:7], v[6:7], v[34:35]
	v_pk_fma_f32 v[28:29], v[84:85], s[24:25], v[8:9] op_sel_hi:[1,0,1]
	v_pk_mul_f32 v[6:7], v[32:33], v[6:7]
	v_med3_f32 v28, v28, s69, v219
	v_cvt_pk_fp8_f32 v31, v6, v7
	v_med3_f32 v29, v29, s69, v219
	v_pk_add_f32 v[6:7], v[28:29], 1.0 op_sel_hi:[1,0]
	v_pk_mul_f32 v[2:3], v[2:3], v[36:37]
	v_add_u32_e32 v27, 0xa0, v26
	v_pk_mul_f32 v[2:3], v[6:7], v[2:3]
	v_pk_fma_f32 v[6:7], v[78:79], s[24:25], v[24:25] op_sel_hi:[1,0,1]
	v_cvt_pk_fp8_f32 v31, v2, v3 op_sel:[0,0,1]
	v_mad_i64_i32 v[2:3], s[36:37], v27, s68, v[20:21]
	v_lshl_add_u64 v[2:3], v[2:3], 0, v[18:19]
	v_min_f32_e32 v6, 0x40e00000, v6
	v_min_f32_e32 v7, 0x40e00000, v7
	global_store_dwordx2 v[2:3], v[30:31], off
	v_pk_fma_f32 v[2:3], v[80:81], s[24:25], v[22:23] op_sel_hi:[1,0,1]
	v_mul_f32_e32 v22, 0xc01d265f, v6
	v_mul_f32_e32 v23, 0xc01d265f, v7
	v_exp_f32_e32 v22, v22
	v_exp_f32_e32 v23, v23
	v_min_f32_e32 v2, 0x40e00000, v2
	v_min_f32_e32 v3, 0x40e00000, v3
	v_mul_f32_e32 v24, 0xc01d265f, v2
	v_mul_f32_e32 v25, 0xc01d265f, v3
	v_exp_f32_e32 v24, v24
	v_exp_f32_e32 v25, v25
	v_pk_add_f32 v[22:23], v[22:23], 1.0 op_sel_hi:[1,0]
	v_pk_fma_f32 v[12:13], v[74:75], s[24:25], v[12:13] op_sel_hi:[1,0,1]
	v_rcp_f32_e32 v22, v22
	v_rcp_f32_e32 v23, v23
	v_pk_add_f32 v[24:25], v[24:25], 1.0 op_sel_hi:[1,0]
	v_med3_f32 v12, v12, s69, v219
	v_med3_f32 v13, v13, s69, v219
	v_rcp_f32_e32 v24, v24
	v_rcp_f32_e32 v25, v25
	v_pk_add_f32 v[12:13], v[12:13], 1.0 op_sel_hi:[1,0]
	v_pk_mul_f32 v[6:7], v[6:7], v[22:23]
	v_pk_fma_f32 v[16:17], v[76:77], s[24:25], v[16:17] op_sel_hi:[1,0,1]
	v_pk_mul_f32 v[6:7], v[12:13], v[6:7]
	v_mov_b32_e32 v12, v197
	v_med3_f32 v16, v16, s69, v219
	v_med3_f32 v17, v17, s69, v219
	v_cvt_pk_fp8_f32 v12, v6, v7
	v_pk_add_f32 v[6:7], v[16:17], 1.0 op_sel_hi:[1,0]
	v_pk_mul_f32 v[2:3], v[2:3], v[24:25]
	v_pk_fma_f32 v[4:5], v[66:67], s[24:25], v[4:5] op_sel_hi:[1,0,1]
	v_pk_mul_f32 v[2:3], v[6:7], v[2:3]
	v_pk_fma_f32 v[6:7], v[70:71], s[24:25], v[14:15] op_sel_hi:[1,0,1]
	v_cvt_pk_fp8_f32 v12, v2, v3 op_sel:[0,0,1]
	v_min_f32_e32 v6, 0x40e00000, v6
	v_min_f32_e32 v7, 0x40e00000, v7
	v_pk_fma_f32 v[2:3], v[72:73], s[24:25], v[10:11] op_sel_hi:[1,0,1]
	v_mul_f32_e32 v10, 0xc01d265f, v6
	v_mul_f32_e32 v11, 0xc01d265f, v7
	v_exp_f32_e32 v10, v10
	v_exp_f32_e32 v11, v11
	v_min_f32_e32 v2, 0x40e00000, v2
	v_min_f32_e32 v3, 0x40e00000, v3
	v_mul_f32_e32 v13, 0xc01d265f, v2
	v_exp_f32_e32 v14, v13
	v_mul_f32_e32 v13, 0xc01d265f, v3
	v_exp_f32_e32 v15, v13
	v_pk_add_f32 v[10:11], v[10:11], 1.0 op_sel_hi:[1,0]
	v_med3_f32 v4, v4, s69, v219
	v_rcp_f32_e32 v10, v10
	v_rcp_f32_e32 v11, v11
	v_med3_f32 v5, v5, s69, v219
	v_pk_add_f32 v[14:15], v[14:15], 1.0 op_sel_hi:[1,0]
	v_pk_add_f32 v[4:5], v[4:5], 1.0 op_sel_hi:[1,0]
	v_rcp_f32_e32 v14, v14
	v_rcp_f32_e32 v15, v15
	v_pk_mul_f32 v[6:7], v[6:7], v[10:11]
	v_mov_b32_e32 v13, v197
	v_pk_mul_f32 v[4:5], v[4:5], v[6:7]
	v_pk_fma_f32 v[8:9], v[68:69], s[24:25], v[8:9] op_sel_hi:[1,0,1]
	v_cvt_pk_fp8_f32 v13, v4, v5
	v_med3_f32 v8, v8, s69, v219
	v_med3_f32 v9, v9, s69, v219
	v_pk_add_f32 v[4:5], v[8:9], 1.0 op_sel_hi:[1,0]
	v_pk_mul_f32 v[2:3], v[2:3], v[14:15]
	v_add_u32_e32 v26, 0xb0, v26
	v_pk_mul_f32 v[2:3], v[4:5], v[2:3]
	s_and_b64 vcc, exec, s[2:3]
	v_cvt_pk_fp8_f32 v13, v2, v3 op_sel:[0,0,1]
	v_mad_i64_i32 v[2:3], s[36:37], v26, s68, v[20:21]
	v_lshl_add_u64 v[2:3], v[2:3], 0, v[18:19]
	s_mov_b64 s[2:3], -1
	global_store_dwordx2 v[2:3], v[12:13], off
	s_cbranch_vccnz .LBB0_922
	s_andn2_b64 vcc, exec, s[16:17]
	s_cbranch_vccnz .LBB0_921
	s_barrier
	s_branch .LBB0_921

; #define LAS __attribute__((address_space(3)))
; #define PG8_STAGE(bufoff, gbase, voff) do { _Pragma("unroll") for (int _i = 0; _i < 2; ++_i) \
;         __builtin_amdgcn_global_load_lds((const unsigned*)((const char*)(gbase) + (voff)[_i]), (LAS unsigned*)(lds + (bufoff) + ldsw + _i * 8192), 16, 0, 0); } while (0)
; #define PG8_WAIT_V(n) asm volatile("s_waitcnt vmcnt(" #n ")" ::: "memory")
; #define PG8_BAR __builtin_amdgcn_s_barrier()
; template <class Epi, class Sched, bool GATHER, bool FP8>
; __device__ __forceinline__ void gemm_phase(LAS uchar* lds, const int K, const int LDA, const int LDB, const size_t kstepA, const size_t kstepB, const Sched& S, const Epi& E) {
;     ...
;     const char* cA = cur.pa; const char* cB = cur.pb;
;     if constexpr (GATHER) S.gather(cur, voA, (const LAS int*)nullptr);
;     PG8_STAGE(PG8_SB(0, 0), cB, voffB); PG8_STAGE(PG8_SB(0, 1), cB + hstep, voffB); PG8_STAGE(PG8_SA(0, 0), cA, voA[0]); PG8_STAGE(PG8_SA(0, 1), cA, voA[1]);
;     if (wr == 1) PG8_BAR;
;     PG8_WAIT_V(2); PG8_BAR;
;     PG8_STAGE(PG8_SB(1, 0), cB + kstepB, voffB); PG8_STAGE(PG8_SA(1, 0), cA + kstepA, voA[0]); PG8_STAGE(PG8_SB(1, 1), cB + hstep + kstepB, voffB);
;     PG8_WAIT_V(6); PG8_BAR;
;     __device__ __forceinline__ bool next(int i, pg8::Unit& u) const {
;         const int NB = __builtin_amdgcn_readfirstlane(tab[0]); const int L = i * G + c; if (L >= NB * nN) return false;
;         const int b = L / nN, pn = L - b * nN, e = __builtin_amdgcn_readfirstlane(tab[64 + b]);
;         u.pa = A; u.pb = B + (size_t)e * bexp + (size_t)pn * 256 * 128; u.row0 = b * 256; u.col0 = pn * 256; u.aux = e; u.blk = b; return true;
;     }
;     __device__ __forceinline__ void gather(const pg8::Unit& u, unsigned (&vo)[2][2], const LAS int*) const {
; #pragma unroll
;         for (int i = 0; i < 2; ++i) { int R, C; pg8::stage_rc((int)threadIdx.x * 16 + i * 8192, R, C);
; #pragma unroll
;             for (int h = 0; h < 2; ++h) vo[h][i] = (unsigned)(u.row0 + h * 128 + R) * (unsigned)W8LD + (unsigned)C * 2u; }
;     }
.LBB0_1022:
	s_add_i32 s4, 0, 0x22000
	v_mov_b32_e32 v2, s4
	ds_read_b32 v2, v2
	v_readfirstlane_b32 s18, v0
	s_waitcnt lgkmcnt(0)
	v_readfirstlane_b32 s4, v2
	s_lshl_b32 s4, s4, 3
	s_and_b32 s98, s87, 7
	s_lshl_b32 s98, s98, 5
	s_lshr_b32 s99, s87, 3
	s_or_b32 s98, s98, s99
	s_cmpk_eq_i32 s92, 0x100
	s_cselect_b32 s98, s98, s87
	s_cmp_ge_i32 s98, s4
	s_cbranch_scc1 .LBB0_1041
	v_lshlrev_b32_e32 v3, 4, v0
	v_and_b32_e32 v2, 32, v0
	v_bitop3_b32 v2, v3, v2, 48 bitop3:0x6c
	v_or_b32_e32 v3, 0x2000, v3
	v_bfe_u32 v5, v0, 2, 4
	v_lshrrev_b32_e32 v6, 7, v3
	s_movk_i32 s8, 0x70
	s_add_u32 s4, s90, 0x1c000000
	v_and_or_b32 v216, v6, s8, v5
	v_lshrrev_b32_e32 v6, 5, v0
	s_addc_u32 s5, s91, 0
	v_and_or_b32 v195, v0, 64, v2
	v_and_b32_e32 v2, 48, v0
	v_and_b32_e32 v6, 4, v6
	v_bfe_u32 v7, v0, 2, 2
	s_add_u32 s23, s90, 0x50000000
	v_or3_b32 v6, v7, v6, v2
	v_lshrrev_b32_e32 v3, 6, v3
	s_movk_i32 s8, 0xc0
	s_addc_u32 s33, s91, 0
	v_and_or_b32 v3, v3, s8, v6
	s_ashr_i32 s8, s98, 31
	s_lshr_b32 s8, s8, 29
	s_add_i32 s8, s98, s8
	s_ashr_i32 s10, s8, 3
	s_lshl_b32 s9, s10, 2
	s_add_i32 s9, s9, 0
	s_add_i32 s9, s9, 0x22100
	v_lshl_or_b32 v196, v3, 7, v195
	v_mov_b32_e32 v3, s9
	ds_read_b32 v3, v3
	s_lshr_b32 s16, s18, 6
	s_and_b32 s8, s8, -8
	s_lshr_b32 s17, s18, 8
	s_lshl_b32 s44, s16, 10
	s_waitcnt lgkmcnt(0)
	v_readfirstlane_b32 s34, v3
	s_ashr_i32 s35, s34, 31
	s_sub_i32 s14, s98, s8
	s_lshl_b64 s[8:9], s[34:35], 22
	s_add_u32 s11, s23, s8
	s_addc_u32 s12, s33, s9
	s_ashr_i32 s15, s14, 31
	s_lshl_b64 s[8:9], s[14:15], 15
	v_lshrrev_b32_e32 v4, 2, v0
	s_add_u32 s36, s11, s8
	v_and_or_b32 v4, v4, 64, v6
	s_addc_u32 s37, s12, s9
	s_lshl_b32 s69, s10, 8
	v_lshl_or_b32 v198, v4, 7, v195
	s_movk_i32 s45, 0x80
	v_or_b32_e32 v4, s69, v216
	v_mul_lo_u32 v4, v4, s45
	v_or_b32_e32 v219, 0x80, v216
	s_add_i32 s46, s44, 0
	v_or_b32_e32 v202, v4, v195
	v_or_b32_e32 v4, s69, v219
	s_add_i32 s47, s46, 0x10000
	v_mov_b32_e32 v201, 0
	v_lshrrev_b32_e32 v3, 3, v0
	v_mul_lo_u32 v4, v4, s45
	v_mov_b32_e32 v199, v201
	s_mov_b32 m0, s47
	s_add_i32 s48, s46, 0x12000
	v_and_or_b32 v217, v3, 48, v5
	v_or_b32_e32 v204, v4, v195
	v_lshl_add_u64 v[4:5], s[36:37], 0, v[198:199]
	global_load_lds_dwordx4 v198, s[36:37]
	v_mov_b32_e32 v197, v201
	s_mov_b32 m0, s48
	s_add_i32 s49, s46, 0x14000
	s_mov_b64 s[8:9], 0x400
	v_or_b32_e32 v3, s69, v217
	v_lshl_add_u64 v[6:7], s[36:37], 0, v[196:197]
	global_load_lds_dwordx4 v196, s[36:37]
	v_lshl_add_u64 v[4:5], v[4:5], 0, s[8:9]
	s_mov_b32 m0, s49
	s_add_i32 s50, s46, 0x16000
	v_mul_lo_u32 v3, v3, s45
	v_or_b32_e32 v218, 0x80, v217
	global_load_lds_dwordx4 v[4:5], off
	v_lshl_add_u64 v[4:5], v[6:7], 0, s[8:9]
	s_mov_b32 m0, s50
	v_or_b32_e32 v200, v3, v195
	v_or_b32_e32 v3, s69, v218
	global_load_lds_dwordx4 v[4:5], off
	s_mov_b32 m0, s46
	s_add_i32 s51, s46, 0x2000
	v_mul_lo_u32 v3, v3, s45
	global_load_lds_dwordx4 v200, s[4:5]
	s_mov_b32 m0, s51
	s_add_i32 s52, s46, 0x4000
	v_or_b32_e32 v3, v3, v195
	global_load_lds_dwordx4 v202, s[4:5]
	s_mov_b32 m0, s52
	s_add_i32 s53, s46, 0x6000
	global_load_lds_dwordx4 v3, s[4:5]
	s_mov_b32 m0, s53
	s_load_dwordx2 s[10:11], s[0:1], 0x88
	global_load_lds_dwordx4 v204, s[4:5]
	s_cmp_eq_u32 s17, 1
	s_mov_b32 s54, 0x10000
	s_cselect_b64 s[12:13], -1, 0
	s_cmp_lg_u32 s17, 1
	v_mov_b32_e32 v203, v201
	s_cbranch_scc1 .LBB0_1025
	s_barrier
.LBB0_1025:
	s_lshl_b32 s30, s14, 8
	s_add_u32 s14, s90, 0x26000000
	s_addc_u32 s15, s91, 0
	s_and_b32 s19, s16, 3
	s_lshl_b32 s55, s17, 6
	s_lshl_b32 s20, s17, 13
	s_lshl_b32 s21, s19, 12
	s_add_u32 s16, s36, 0x40000
	s_addc_u32 s17, s37, 0
	s_add_i32 m0, s46, 0x18000
	v_lshl_add_u64 v[4:5], s[16:17], 0, v[198:199]
	s_waitcnt vmcnt(2)
	s_barrier
	global_load_lds_dwordx4 v[4:5], off
	s_add_i32 m0, s46, 0x1a000
	v_lshl_add_u64 v[4:5], s[16:17], 0, v[196:197]
	s_add_u32 s16, s90, 0x1c500000
	s_addc_u32 s17, s91, 0
	s_add_i32 s56, s46, 0x8000
	global_load_lds_dwordx4 v[4:5], off
	v_lshl_add_u64 v[4:5], s[16:17], 0, v[200:201]
	s_mov_b32 m0, s56
	s_add_i32 s57, s46, 0xa000
	global_load_lds_dwordx4 v[4:5], off
	v_lshl_add_u64 v[4:5], s[16:17], 0, v[202:203]
	s_add_u32 s16, s36, 0x40400
	s_mov_b32 m0, s57
	s_addc_u32 s17, s37, 0
	global_load_lds_dwordx4 v[4:5], off
	s_add_i32 m0, s46, 0x1c000
	v_lshl_add_u64 v[4:5], s[16:17], 0, v[198:199]
	global_load_lds_dwordx4 v[4:5], off
	v_lshl_add_u64 v[4:5], s[16:17], 0, v[196:197]
	s_add_i32 m0, s46, 0x1e000
	s_movk_i32 s16, 0x3c0
	global_load_lds_dwordx4 v[4:5], off
	v_lshlrev_b32_e32 v4, 6, v0
	v_and_or_b32 v2, v4, s16, v2
	v_lshlrev_b32_e32 v4, 2, v0
	v_and_b32_e32 v4, 32, v4
	s_lshl_b32 s60, s19, 6
	s_lshl_b32 s61, s19, 8
	v_bitop3_b32 v220, s21, v2, v4 bitop3:0xf6
	s_waitcnt vmcnt(6)
	s_cmpk_lt_u32 s18, 0x100
	v_bitop3_b32 v5, v2, s20, v4 bitop3:0xde
	s_cselect_b64 s[18:19], -1, 0
	s_add_i32 s20, 0, 0x22000
	v_add_u32_e32 v2, 0, v220
	s_mov_b32 s38, 0
	s_mov_b32 s58, 0x18000
	s_mov_b64 s[16:17], 0x1c500000
	s_mov_b32 s59, 0x8000
	v_mov_b32_e32 v221, s20
	s_lshl_b32 s62, s60, 2
	v_lshlrev_b32_e32 v222, 2, v194
	v_add_u32_e32 v223, 0x10000, v2
	v_add_u32_e32 v224, 0x14000, v2
	v_add_u32_e32 v225, 0, v5
	v_mov_b32_e32 v226, 0x7f7f7f7f
	s_mov_b64 s[20:21], 0x500000
	s_mov_b32 s22, 0x3c800000
	s_mov_b32 s63, 0xc3e00000
	s_mov_b32 s64, 0x40000
	s_mov_b32 s65, 0x48000
	s_mov_b32 s66, 0x50000
	v_mov_b32_e32 v227, 0x43e00000
	v_mov_b32_e32 v206, v200
	v_mov_b32_e32 v200, v3
	s_mov_b64 s[26:27], s[36:37]
	s_barrier
	s_branch .LBB0_1028

; template <class Epi, class Sched, bool GATHER, bool FP8>
; __device__ __forceinline__ void gemm_phase(LAS uchar* lds, const int K, const int LDA, const int LDB, const size_t kstepA, const size_t kstepB, const Sched& S, const Epi& E) {
;     ...
;         const bool has_next = S.next(ui + 1, nxt);
;         if constexpr (GATHER) { if (has_next) S.prefetch(nxt, lds + LDS_IDX + ((ui + 1) & 1) * 1024, wid, lane); }
;         E.prefetch(cur, lds + LDS_BIAS + (ui & 1) * 1024, wid, lane);
;         const char* nA = has_next ? nxt.pa : cA; const char* nB = has_next ? nxt.pb : cB;
;     __device__ __forceinline__ bool next(int i, pg8::Unit& u) const {
;         const int NB = __builtin_amdgcn_readfirstlane(tab[0]); const int L = i * G + c; if (L >= NB * nN) return false;
;         const int b = L / nN, pn = L - b * nN, e = __builtin_amdgcn_readfirstlane(tab[64 + b]);
;         u.pa = A; u.pb = B + (size_t)e * bexp + (size_t)pn * 256 * 128; u.row0 = b * 256; u.col0 = pn * 256; u.aux = e; u.blk = b; return true;
.LBB0_1028:
	ds_read_b32 v2, v221
	s_add_i32 s67, s38, 1
	s_mul_i32 s31, s67, s92
	s_add_i32 s31, s31, s98
	s_waitcnt lgkmcnt(0)
	v_readfirstlane_b32 s28, v2
	s_lshl_b32 s35, s28, 3
	s_cmp_lt_i32 s31, s35
	s_cselect_b64 s[28:29], -1, 0
	s_cmp_ge_i32 s31, s35
	s_cbranch_scc1 .LBB0_1030
	s_ashr_i32 s24, s31, 31
	s_lshr_b32 s24, s24, 29
	s_add_i32 s24, s31, s24
	s_ashr_i32 s35, s24, 3
	s_lshl_b32 s25, s35, 2
	s_add_i32 s25, s25, 0
	s_add_i32 s25, s25, 0x22100
	v_mov_b32_e32 v2, s25
	ds_read_b32 v2, v2
	s_and_b32 s24, s24, -8
	s_sub_i32 s40, s31, s24
	s_waitcnt lgkmcnt(0)
	v_readfirstlane_b32 s24, v2
	s_ashr_i32 s25, s24, 31
	s_lshl_b64 s[26:27], s[24:25], 22
	s_add_u32 s25, s23, s26
	s_addc_u32 s31, s33, s27
	s_ashr_i32 s41, s40, 31
	s_lshl_b64 s[26:27], s[40:41], 15
	s_add_u32 s26, s25, s26
	s_addc_u32 s27, s31, s27
	s_lshl_b32 s68, s35, 8
	s_lshl_b32 s25, s40, 8

; #define LAS __attribute__((address_space(3)))
; #define PG8_STAGE(bufoff, gbase, voff) do { _Pragma("unroll") for (int _i = 0; _i < 2; ++_i) \
;         __builtin_amdgcn_global_load_lds((const unsigned*)((const char*)(gbase) + (voff)[_i]), (LAS unsigned*)(lds + (bufoff) + ldsw + _i * 8192), 16, 0, 0); } while (0)
; #define PG8_LDA(dst, b, h) do { _Pragma("unroll") for (int m = 0; m < 4; ++m) _Pragma("unroll") for (int k = 0; k < 2; ++k) dst[m][k] = *(const LAS bf16x8*)(lds + PG8_SA(b, h) + aoff + m * 2048 + k * 1024); } while (0)
; #define PG8_LDB(dst, b, h) do { _Pragma("unroll") for (int n = 0; n < 2; ++n) _Pragma("unroll") for (int k = 0; k < 2; ++k) dst[n][k] = *(const LAS bf16x8*)(lds + PG8_SB(b, h) + boff + n * 2048 + k * 1024); } while (0)
; #define PG8_WAIT_V8F(fresh) asm volatile("s_cmp_eq_u32 %0, 0\n\ts_cbranch_scc1 .Lw8_%=\n\ts_waitcnt vmcnt(%1)\n\ts_branch .Lwe_%=\n.Lw8_%=:\n\ts_waitcnt vmcnt(8)\n.Lwe_%=:" :: "s"(fresh), "n"(8 + Epi::NST + Epi::NPF) : "memory", "scc")
; #define PG8_WAIT_L(n) asm volatile("s_waitcnt lgkmcnt(" #n ")" ::: "memory")
; #define PG8_BAR __builtin_amdgcn_s_barrier()
; #define PG8_SCHED __builtin_amdgcn_sched_barrier(0)
; template <class Epi, class Sched, bool GATHER, bool FP8>
; __device__ __forceinline__ void gemm_phase(LAS uchar* lds, const int K, const int LDA, const int LDB, const size_t kstepA, const size_t kstepB, const Sched& S, const Epi& E) {
;     ...
;             const bool last = (t == nt - 2);
;             const char* a1 = cA + (size_t)(t + 1) * kstepA;
;             const char* a2 = last ? nA : cA + (size_t)(t + 2) * kstepA; const char* b2 = last ? nB : cB + (size_t)(t + 2) * kstepB;
;             const char* a3 = a2 + kstepA; const char* b3 = b2 + kstepB;
;             int fresh; { const int fv = (t == 0 && ui > 0) ? 1 : 0; asm volatile("s_nop 0\n\tv_readfirstlane_b32 %0, %1" : "=s"(fresh) : "v"(fv)); }
;             PG8_LDB(B0, 0, 0); PG8_LDB(B1, 0, 1); PG8_SCHED; PG8_LDA(At, 0, 0); PG8_STAGE(PG8_SA(1, 1), a1, voA[1]);
;             if constexpr (GATHER) { if (last && has_next) S.gather(nxt, voA, (const LAS int*)(lds + LDS_IDX + ((ui + 1) & 1) * 1024)); }
;             PG8_WAIT_V8F(fresh); PG8_WAIT_L(0); PG8_BAR; PG8_MMA(0, 0, At, B0); PG8_MMA(0, 1, At, B1); PG8_BAR; PG8_SCHED;
.LBB0_1032:
	s_add_u32 s40, s90, s36
	s_addc_u32 s41, s91, s37
	s_add_u32 s40, s40, 0x1ca00000
	s_addc_u32 s41, s41, 0
	s_and_b64 s[38:39], s[38:39], exec
	s_cselect_b32 s38, s26, s31
	s_cselect_b32 s43, s5, s41
	s_cselect_b32 s42, s4, s40
	s_cselect_b32 s39, s27, s71
	s_add_u32 s40, s38, 0x40000
	s_addc_u32 s41, s39, 0
	s_cmp_eq_u32 s73, 0
	s_cbranch_scc1 .Lw8_6
	s_waitcnt vmcnt(17)
	s_branch .Lwe_6

; #define PG8_STAGE(bufoff, gbase, voff) do { _Pragma("unroll") for (int _i = 0; _i < 2; ++_i) \
;         __builtin_amdgcn_global_load_lds((const unsigned*)((const char*)(gbase) + (voff)[_i]), (LAS unsigned*)(lds + (bufoff) + ldsw + _i * 8192), 16, 0, 0); } while (0)
; #define PG8_LDA(dst, b, h) do { _Pragma("unroll") for (int m = 0; m < 4; ++m) _Pragma("unroll") for (int k = 0; k < 2; ++k) dst[m][k] = *(const LAS bf16x8*)(lds + PG8_SA(b, h) + aoff + m * 2048 + k * 1024); } while (0)
; #define PG8_LDB(dst, b, h) do { _Pragma("unroll") for (int n = 0; n < 2; ++n) _Pragma("unroll") for (int k = 0; k < 2; ++k) dst[n][k] = *(const LAS bf16x8*)(lds + PG8_SB(b, h) + boff + n * 2048 + k * 1024); } while (0)
; #define PG8_WAIT_V(n) asm volatile("s_waitcnt vmcnt(" #n ")" ::: "memory")
; #define PG8_WAIT_V8F(fresh) asm volatile("s_cmp_eq_u32 %0, 0\n\ts_cbranch_scc1 .Lw8_%=\n\ts_waitcnt vmcnt(%1)\n\ts_branch .Lwe_%=\n.Lw8_%=:\n\ts_waitcnt vmcnt(8)\n.Lwe_%=:" :: "s"(fresh), "n"(8 + Epi::NST + Epi::NPF) : "memory", "scc")
; #define PG8_WAIT_L(n) asm volatile("s_waitcnt lgkmcnt(" #n ")" ::: "memory")
; #define PG8_BAR __builtin_amdgcn_s_barrier()
; #define PG8_SCHED __builtin_amdgcn_sched_barrier(0)
; template <class Epi, class Sched, bool GATHER, bool FP8>
; __device__ __forceinline__ void gemm_phase(LAS uchar* lds, const int K, const int LDA, const int LDB, const size_t kstepA, const size_t kstepB, const Sched& S, const Epi& E) {
;     ...
;             PG8_WAIT_V8F(fresh); PG8_WAIT_L(0); PG8_BAR; PG8_MMA(1, 0, At, B0); PG8_MMA(1, 1, At, B1); PG8_BAR; PG8_SCHED;
;             PG8_LDB(B0, 1, 0); PG8_LDB(B1, 1, 1); PG8_SCHED; PG8_LDA(At, 1, 0); PG8_STAGE(PG8_SA(0, 1), a2, voA[1]);
;             PG8_WAIT_V(8); PG8_WAIT_L(0); PG8_BAR; PG8_MMA(0, 0, At, B0); PG8_MMA(0, 1, At, B1); PG8_BAR; PG8_SCHED;
.Lwe_7:
	s_waitcnt lgkmcnt(0)
	s_barrier
	s_setprio 1
	s_waitcnt lgkmcnt(0)
	v_mfma_scale_f32_16x16x128_f8f6f4 v[126:129], v[18:25], v[34:41], v[126:129], v226, v226 op_sel_hi:[0,0,0]
	v_mfma_scale_f32_16x16x128_f8f6f4 v[122:125], v[26:33], v[34:41], v[122:125], v226, v226 op_sel_hi:[0,0,0]
	v_mfma_scale_f32_16x16x128_f8f6f4 v[110:113], v[18:25], v[42:49], v[110:113], v226, v226 op_sel_hi:[0,0,0]
	v_mfma_scale_f32_16x16x128_f8f6f4 v[106:109], v[26:33], v[42:49], v[106:109], v226, v226 op_sel_hi:[0,0,0]
	v_mfma_scale_f32_16x16x128_f8f6f4 v[94:97], v[18:25], v[50:57], v[94:97], v226, v226 op_sel_hi:[0,0,0]
	v_mfma_scale_f32_16x16x128_f8f6f4 v[90:93], v[26:33], v[50:57], v[90:93], v226, v226 op_sel_hi:[0,0,0]
	v_mfma_scale_f32_16x16x128_f8f6f4 v[78:81], v[18:25], v[58:65], v[78:81], v226, v226 op_sel_hi:[0,0,0]
	v_mfma_scale_f32_16x16x128_f8f6f4 v[74:77], v[26:33], v[58:65], v[74:77], v226, v226 op_sel_hi:[0,0,0]
	s_setprio 0
	s_setprio 1
	v_mfma_scale_f32_16x16x128_f8f6f4 v[118:121], v[2:9], v[34:41], v[118:121], v226, v226 op_sel_hi:[0,0,0]
	v_mfma_scale_f32_16x16x128_f8f6f4 v[114:117], v[10:17], v[34:41], v[114:117], v226, v226 op_sel_hi:[0,0,0]
	v_mfma_scale_f32_16x16x128_f8f6f4 v[102:105], v[2:9], v[42:49], v[102:105], v226, v226 op_sel_hi:[0,0,0]
	v_mfma_scale_f32_16x16x128_f8f6f4 v[98:101], v[10:17], v[42:49], v[98:101], v226, v226 op_sel_hi:[0,0,0]
	v_mfma_scale_f32_16x16x128_f8f6f4 v[86:89], v[2:9], v[50:57], v[86:89], v226, v226 op_sel_hi:[0,0,0]
	v_mfma_scale_f32_16x16x128_f8f6f4 v[82:85], v[10:17], v[50:57], v[82:85], v226, v226 op_sel_hi:[0,0,0]
	v_mfma_scale_f32_16x16x128_f8f6f4 v[70:73], v[2:9], v[58:65], v[70:73], v226, v226 op_sel_hi:[0,0,0]
	v_mfma_scale_f32_16x16x128_f8f6f4 v[66:69], v[10:17], v[58:65], v[66:69], v226, v226 op_sel_hi:[0,0,0]
	s_setprio 0
	s_barrier
	s_add_i32 s73, 0, 0x18000
	s_add_i32 s74, 0, 0x1c000
	v_add_u32_e32 v14, s73, v220
	v_add_u32_e32 v30, s74, v220
	ds_read_b128 v[2:5], v14
	ds_read_b128 v[6:9], v14 offset:1024
	ds_read_b128 v[10:13], v14 offset:2048
	ds_read_b128 v[14:17], v14 offset:3072
	ds_read_b128 v[18:21], v30
	ds_read_b128 v[22:25], v30 offset:1024
	ds_read_b128 v[26:29], v30 offset:2048
	ds_read_b128 v[30:33], v30 offset:3072
	s_mov_b32 m0, s52
	v_lshl_add_u64 v[214:215], s[42:43], 0, v[214:215]
	ds_read_b128 v[34:37], v225 offset:32768
	ds_read_b128 v[38:41], v225 offset:33792
	ds_read_b128 v[42:45], v225 offset:34816
	ds_read_b128 v[46:49], v225 offset:35840
	ds_read_b128 v[50:53], v225 offset:36864
	ds_read_b128 v[54:57], v225 offset:37888
	ds_read_b128 v[58:61], v225 offset:38912
	ds_read_b128 v[62:65], v225 offset:39936
	global_load_lds_dwordx4 v[214:215], off
	v_lshl_add_u64 v[212:213], s[42:43], 0, v[212:213]
	s_mov_b32 m0, s53
	s_nop 0
	global_load_lds_dwordx4 v[212:213], off
	s_waitcnt vmcnt(8)
	s_waitcnt lgkmcnt(0)
	s_barrier
	s_setprio 1
	s_waitcnt lgkmcnt(0)
	v_mfma_scale_f32_16x16x128_f8f6f4 v[190:193], v[2:9], v[34:41], v[190:193], v226, v226 op_sel_hi:[0,0,0]
	v_mfma_scale_f32_16x16x128_f8f6f4 v[186:189], v[10:17], v[34:41], v[186:189], v226, v226 op_sel_hi:[0,0,0]
	v_mfma_scale_f32_16x16x128_f8f6f4 v[174:177], v[2:9], v[42:49], v[174:177], v226, v226 op_sel_hi:[0,0,0]
	v_mfma_scale_f32_16x16x128_f8f6f4 v[170:173], v[10:17], v[42:49], v[170:173], v226, v226 op_sel_hi:[0,0,0]
	v_mfma_scale_f32_16x16x128_f8f6f4 v[158:161], v[2:9], v[50:57], v[158:161], v226, v226 op_sel_hi:[0,0,0]
	v_mfma_scale_f32_16x16x128_f8f6f4 v[154:157], v[10:17], v[50:57], v[154:157], v226, v226 op_sel_hi:[0,0,0]
	v_mfma_scale_f32_16x16x128_f8f6f4 v[142:145], v[2:9], v[58:65], v[142:145], v226, v226 op_sel_hi:[0,0,0]
	v_mfma_scale_f32_16x16x128_f8f6f4 v[138:141], v[10:17], v[58:65], v[138:141], v226, v226 op_sel_hi:[0,0,0]
	s_setprio 0
	s_setprio 1
	v_mfma_scale_f32_16x16x128_f8f6f4 v[182:185], v[18:25], v[34:41], v[182:185], v226, v226 op_sel_hi:[0,0,0]
	v_mfma_scale_f32_16x16x128_f8f6f4 v[178:181], v[26:33], v[34:41], v[178:181], v226, v226 op_sel_hi:[0,0,0]
	v_mfma_scale_f32_16x16x128_f8f6f4 v[166:169], v[18:25], v[42:49], v[166:169], v226, v226 op_sel_hi:[0,0,0]
	v_mfma_scale_f32_16x16x128_f8f6f4 v[162:165], v[26:33], v[42:49], v[162:165], v226, v226 op_sel_hi:[0,0,0]
	v_mfma_scale_f32_16x16x128_f8f6f4 v[150:153], v[18:25], v[50:57], v[150:153], v226, v226 op_sel_hi:[0,0,0]
	v_mfma_scale_f32_16x16x128_f8f6f4 v[146:149], v[26:33], v[50:57], v[146:149], v226, v226 op_sel_hi:[0,0,0]
	v_mfma_scale_f32_16x16x128_f8f6f4 v[134:137], v[18:25], v[58:65], v[134:137], v226, v226 op_sel_hi:[0,0,0]
	v_mfma_scale_f32_16x16x128_f8f6f4 v[130:133], v[26:33], v[58:65], v[130:133], v226, v226 op_sel_hi:[0,0,0]
	s_setprio 0
	s_barrier
; #define LAS __attribute__((address_space(3)))
; #define PG8_STAGE(bufoff, gbase, voff) do { _Pragma("unroll") for (int _i = 0; _i < 2; ++_i) \
;         __builtin_amdgcn_global_load_lds((const unsigned*)((const char*)(gbase) + (voff)[_i]), (LAS unsigned*)(lds + (bufoff) + ldsw + _i * 8192), 16, 0, 0); } while (0)
; #define PG8_WAIT_V(n) asm volatile("s_waitcnt vmcnt(" #n ")" ::: "memory")
; #define PG8_WAIT_L(n) asm volatile("s_waitcnt lgkmcnt(" #n ")" ::: "memory")
; template <class Epi, class Sched, bool GATHER, bool FP8>
; __device__ __forceinline__ void gemm_phase(LAS uchar* lds, const int K, const int LDA, const int LDB, const size_t kstepA, const size_t kstepB, const Sched& S, const Epi& E) {
;     ...
;         for (int t = 0; t < nt; t += 2) {
;             const bool last = (t == nt - 2);
;             const char* a1 = cA + (size_t)(t + 1) * kstepA;
;             const char* a2 = last ? nA : cA + (size_t)(t + 2) * kstepA; const char* b2 = last ? nB : cB + (size_t)(t + 2) * kstepB;
;             const char* a3 = a2 + kstepA; const char* b3 = b2 + kstepB;
;             int fresh; { const int fv = (t == 0 && ui > 0) ? 1 : 0; asm volatile("s_nop 0\n\tv_readfirstlane_b32 %0, %1" : "=s"(fresh) : "v"(fv)); }
;             PG8_LDB(B0, 0, 0); PG8_LDB(B1, 0, 1); PG8_SCHED; PG8_LDA(At, 0, 0); PG8_STAGE(PG8_SA(1, 1), a1, voA[1]);
;             if constexpr (GATHER) { if (last && has_next) S.gather(nxt, voA, (const LAS int*)(lds + LDS_IDX + ((ui + 1) & 1) * 1024)); }
;             PG8_WAIT_V8F(fresh); PG8_WAIT_L(0); PG8_BAR; PG8_MMA(0, 0, At, B0); PG8_MMA(0, 1, At, B1); PG8_BAR; PG8_SCHED;
;             PG8_LDA(At, 0, 1); PG8_STAGE(PG8_SB(0, 0), b2, voffB); PG8_STAGE(PG8_SB(0, 1), b2 + hstep, voffB); PG8_STAGE(PG8_SA(0, 0), a2, voA[0]);
;             PG8_WAIT_V8F(fresh); PG8_WAIT_L(0); PG8_BAR; PG8_MMA(1, 0, At, B0); PG8_MMA(1, 1, At, B1); PG8_BAR; PG8_SCHED;
;             PG8_LDB(B0, 1, 0); PG8_LDB(B1, 1, 1); PG8_SCHED; PG8_LDA(At, 1, 0); PG8_STAGE(PG8_SA(0, 1), a2, voA[1]);
;             PG8_WAIT_V(8); PG8_WAIT_L(0); PG8_BAR; PG8_MMA(0, 0, At, B0); PG8_MMA(0, 1, At, B1); PG8_BAR; PG8_SCHED;
;             PG8_LDA(At, 1, 1); PG8_STAGE(PG8_SB(1, 0), b3, voffB); PG8_STAGE(PG8_SB(1, 1), b3 + hstep, voffB); PG8_STAGE(PG8_SA(1, 0), a3, voA[0]);
;             PG8_WAIT_V(8); PG8_WAIT_L(0); PG8_BAR; PG8_MMA(1, 0, At, B0); PG8_MMA(1, 1, At, B1); PG8_BAR; PG8_SCHED;
	s_add_i32 s42, s73, s44
	v_lshl_add_u64 v[212:213], s[40:41], 0, v[198:199]
	s_mov_b32 m0, s42
	ds_read_b128 v[34:37], v225 offset:49152
	ds_read_b128 v[38:41], v225 offset:50176
	ds_read_b128 v[42:45], v225 offset:51200
	ds_read_b128 v[46:49], v225 offset:52224
	ds_read_b128 v[50:53], v225 offset:53248
	ds_read_b128 v[54:57], v225 offset:54272
	ds_read_b128 v[58:61], v225 offset:55296
	ds_read_b128 v[62:65], v225 offset:56320
	global_load_lds_dwordx4 v[212:213], off
	s_add_i32 m0, s42, 0x2000
	s_add_u32 s38, s38, 0x40400
	v_lshl_add_u64 v[212:213], s[40:41], 0, v[196:197]
	s_addc_u32 s39, s39, 0
	s_add_i32 s40, s74, s44
	global_load_lds_dwordx4 v[212:213], off
	v_lshl_add_u64 v[212:213], s[38:39], 0, v[198:199]
	s_mov_b32 m0, s40
	s_nop 0
	global_load_lds_dwordx4 v[212:213], off
	v_lshl_add_u64 v[212:213], s[38:39], 0, v[196:197]
	s_add_i32 m0, s40, 0x2000
	s_nop 0
	global_load_lds_dwordx4 v[212:213], off
	v_lshl_add_u64 v[212:213], v[230:231], 0, s[20:21]
	s_mov_b32 m0, s56
	s_nop 0
	global_load_lds_dwordx4 v[212:213], off
	v_lshl_add_u64 v[212:213], v[232:233], 0, s[20:21]
	s_mov_b32 m0, s57
	s_nop 0
	global_load_lds_dwordx4 v[212:213], off
	s_waitcnt vmcnt(8)
	s_waitcnt lgkmcnt(0)
	s_barrier
	s_setprio 1
	s_waitcnt lgkmcnt(0)
	v_mfma_scale_f32_16x16x128_f8f6f4 v[126:129], v[2:9], v[34:41], v[126:129], v226, v226 op_sel_hi:[0,0,0]
	v_mfma_scale_f32_16x16x128_f8f6f4 v[122:125], v[10:17], v[34:41], v[122:125], v226, v226 op_sel_hi:[0,0,0]
	v_mfma_scale_f32_16x16x128_f8f6f4 v[110:113], v[2:9], v[42:49], v[110:113], v226, v226 op_sel_hi:[0,0,0]
	v_mfma_scale_f32_16x16x128_f8f6f4 v[106:109], v[10:17], v[42:49], v[106:109], v226, v226 op_sel_hi:[0,0,0]
	v_mfma_scale_f32_16x16x128_f8f6f4 v[94:97], v[2:9], v[50:57], v[94:97], v226, v226 op_sel_hi:[0,0,0]
	v_mfma_scale_f32_16x16x128_f8f6f4 v[90:93], v[10:17], v[50:57], v[90:93], v226, v226 op_sel_hi:[0,0,0]
	v_mfma_scale_f32_16x16x128_f8f6f4 v[78:81], v[2:9], v[58:65], v[78:81], v226, v226 op_sel_hi:[0,0,0]
	v_mfma_scale_f32_16x16x128_f8f6f4 v[74:77], v[10:17], v[58:65], v[74:77], v226, v226 op_sel_hi:[0,0,0]
	s_setprio 0
	s_setprio 1
	v_mfma_scale_f32_16x16x128_f8f6f4 v[118:121], v[18:25], v[34:41], v[118:121], v226, v226 op_sel_hi:[0,0,0]
	v_mfma_scale_f32_16x16x128_f8f6f4 v[114:117], v[26:33], v[34:41], v[114:117], v226, v226 op_sel_hi:[0,0,0]
	v_mfma_scale_f32_16x16x128_f8f6f4 v[102:105], v[18:25], v[42:49], v[102:105], v226, v226 op_sel_hi:[0,0,0]
	v_mfma_scale_f32_16x16x128_f8f6f4 v[98:101], v[26:33], v[42:49], v[98:101], v226, v226 op_sel_hi:[0,0,0]
	v_mfma_scale_f32_16x16x128_f8f6f4 v[86:89], v[18:25], v[50:57], v[86:89], v226, v226 op_sel_hi:[0,0,0]
	v_mfma_scale_f32_16x16x128_f8f6f4 v[82:85], v[26:33], v[50:57], v[82:85], v226, v226 op_sel_hi:[0,0,0]
	v_mfma_scale_f32_16x16x128_f8f6f4 v[70:73], v[18:25], v[58:65], v[70:73], v226, v226 op_sel_hi:[0,0,0]
	v_mfma_scale_f32_16x16x128_f8f6f4 v[66:69], v[26:33], v[58:65], v[66:69], v226, v226 op_sel_hi:[0,0,0]
	s_setprio 0
	s_barrier
	s_add_i32 s72, s72, 2
	s_add_u32 s36, s36, 0xa00000
	s_addc_u32 s37, s37, 0
	s_add_u32 s31, s31, 0x80000
	s_addc_u32 s71, s71, 0
	s_cmp_gt_u32 s72, 13
	s_cbranch_scc1 .LBB0_1035
.LBB0_1033:
	s_cmp_eq_u32 s36, 0x4600000
	s_cselect_b64 s[38:39], -1, 0
	s_cmp_eq_u32 s36, 0
	s_cselect_b64 s[40:41], -1, 0
	s_and_b64 s[40:41], s[34:35], s[40:41]
	v_cndmask_b32_e64 v2, 0, 1, s[40:41]
	s_nop 0
	v_readfirstlane_b32 s73, v2
	ds_read_b128 v[18:21], v223
	ds_read_b128 v[22:25], v223 offset:1024
	ds_read_b128 v[26:29], v223 offset:2048
	ds_read_b128 v[30:33], v223 offset:3072
	ds_read_b128 v[2:5], v224
	ds_read_b128 v[6:9], v224 offset:1024
	ds_read_b128 v[10:13], v224 offset:2048
	ds_read_b128 v[14:17], v224 offset:3072
	s_add_u32 s40, s90, s36
	s_addc_u32 s41, s91, s37
	v_lshl_add_u64 v[212:213], s[40:41], 0, v[200:201]
	v_lshl_add_u64 v[212:213], v[212:213], 0, s[16:17]
	s_add_i32 m0, s46, 0xc000
	v_mov_b32_e32 v205, v201
	ds_read_b128 v[58:61], v225
	ds_read_b128 v[62:65], v225 offset:1024
	ds_read_b128 v[50:53], v225 offset:2048
	ds_read_b128 v[54:57], v225 offset:3072
	ds_read_b128 v[42:45], v225 offset:4096
	ds_read_b128 v[46:49], v225 offset:5120
	ds_read_b128 v[34:37], v225 offset:6144
	ds_read_b128 v[38:41], v225 offset:7168
	global_load_lds_dwordx4 v[212:213], off
	v_lshl_add_u64 v[212:213], s[40:41], 0, v[204:205]
	v_lshl_add_u64 v[212:213], v[212:213], 0, s[16:17]
	s_add_i32 m0, s46, 0xe000
	s_and_b64 s[40:41], s[28:29], s[38:39]
	global_load_lds_dwordx4 v[212:213], off
	s_andn2_b64 vcc, exec, s[40:41]
	s_cbranch_vccz .LBB0_1031
	v_mov_b64_e32 v[212:213], v[204:205]
	v_mov_b64_e32 v[214:215], v[200:201]
	s_branch .LBB0_1032

; __global__ void __launch_bounds__(NTHR, 2) fwd(Args args) {
	.amdhsa_kernel _Z3fwd4Args
		.amdhsa_group_segment_fixed_size 0
		.amdhsa_private_segment_fixed_size 0
		.amdhsa_kernarg_size 432
		.amdhsa_user_sgpr_count 2
		.amdhsa_user_sgpr_dispatch_ptr 0
		.amdhsa_user_sgpr_queue_ptr 0
		.amdhsa_user_sgpr_kernarg_segment_ptr 1
		.amdhsa_user_sgpr_dispatch_id 0
		.amdhsa_user_sgpr_kernarg_preload_length 0
		.amdhsa_user_sgpr_kernarg_preload_offset 0
		.amdhsa_user_sgpr_private_segment_size 0
		.amdhsa_uses_dynamic_stack 0
		.amdhsa_enable_private_segment 0
		.amdhsa_system_sgpr_workgroup_id_x 1
		.amdhsa_system_sgpr_workgroup_id_y 0
		.amdhsa_system_sgpr_workgroup_id_z 0
		.amdhsa_system_sgpr_workgroup_info 0
		.amdhsa_system_vgpr_workitem_id 0
		.amdhsa_next_free_vgpr 256
		.amdhsa_next_free_sgpr 102
		.amdhsa_accum_offset 256
		.amdhsa_reserve_vcc 1
		.amdhsa_float_round_mode_32 0
		.amdhsa_float_round_mode_16_64 0
		.amdhsa_float_denorm_mode_32 3
		.amdhsa_float_denorm_mode_16_64 3
		.amdhsa_dx10_clamp 1
		.amdhsa_ieee_mode 1
		.amdhsa_fp16_overflow 0
		.amdhsa_tg_split 0
		.amdhsa_exception_fp_ieee_invalid_op 0
		.amdhsa_exception_fp_denorm_src 0
		.amdhsa_exception_fp_ieee_div_zero 0
		.amdhsa_exception_fp_ieee_overflow 0
		.amdhsa_exception_fp_ieee_underflow 0
		.amdhsa_exception_fp_ieee_inexact 0
		.amdhsa_exception_int_div_zero 0
	.end_amdhsa_kernel

; __global__ void __launch_bounds__(NTHR, 2) fwd(Args args) {
amdhsa.kernels:
  - .agpr_count:     0
    .args:
      - .offset:         0
        .size:           176
        .value_kind:     by_value
      - .offset:         176
        .size:           4
        .value_kind:     hidden_block_count_x
      - .offset:         180
        .size:           4
        .value_kind:     hidden_block_count_y
      - .offset:         184
        .size:           4
        .value_kind:     hidden_block_count_z
      - .offset:         188
        .size:           2
        .value_kind:     hidden_group_size_x
      - .offset:         190
        .size:           2
        .value_kind:     hidden_group_size_y
      - .offset:         192
        .size:           2
        .value_kind:     hidden_group_size_z
      - .offset:         194
        .size:           2
        .value_kind:     hidden_remainder_x
      - .offset:         196
        .size:           2
        .value_kind:     hidden_remainder_y
      - .offset:         198
        .size:           2
        .value_kind:     hidden_remainder_z
      - .offset:         216
        .size:           8
        .value_kind:     hidden_global_offset_x
      - .offset:         224
        .size:           8
        .value_kind:     hidden_global_offset_y
      - .offset:         232
        .size:           8
        .value_kind:     hidden_global_offset_z
      - .offset:         240
        .size:           2
        .value_kind:     hidden_grid_dims
      - .offset:         296
        .size:           4
        .value_kind:     hidden_dynamic_lds_size
    .group_segment_fixed_size: 0
    .kernarg_segment_align: 8
    .kernarg_segment_size: 432
    .language:       OpenCL C
    .language_version:
      - 2
      - 0
    .max_flat_workgroup_size: 512
    .name:           _Z3fwd4Args
    .private_segment_fixed_size: 0
    .sgpr_count:     108
    .sgpr_spill_count: 59
    .symbol:         _Z3fwd4Args.kd
    .uniform_work_group_size: 1
    .uses_dynamic_stack: false
    .vgpr_count:     256
    .vgpr_spill_count: 0
    .wavefront_size: 64
